# adds: uq epilogue rotary cos/sin rows prefetched through a 3-deep ring (counted waits) instead of 4 loads + full wait per row group
# speedup vs baseline: 1.0099x; 1.0099x over previous
; __device__ __forceinline__ float xor32(float x) { auto rr = __builtin_amdgcn_permlane32_swap(__float_as_uint(x), __float_as_uint(x), false, false); return __uint_as_float(((unsigned)(threadIdx.x & 32)) ? rr[0] : rr[1]); }
; __device__ __forceinline__ u32x4 pack8(f32x4 a, f32x4 b) { u32x4 w; w.x = pk2(a[0], a[1]); w.y = pk2(a[2], a[3]); w.z = pk2(b[0], b[1]); w.w = pk2(b[2], b[3]); return w; }
; __device__ __forceinline__ f32x2 rtab_get(LAS unsigned char* lds, int ui, int r) { return ((const LAS f32x2*)(lds + RTAB_OFF))[(ui & 1) * 256 + r]; }
;     __device__ __forceinline__ void operator()(const f32x4 (&acc)[2][2][4][2], const Unit& u, int ui, int wr, int wc, int fr, int fq, LAS unsigned char* lds) const {
;     ...
;             for (int m = 0; m < 4; ++m) {
;                 const int rr = ai * 128 + wr * 64 + m * 16 + fr, row = u.pm * 256 + rr; const float rs = rtab_get(lds, ui, rr)[0];
; #pragma unroll
;                 for (int bj = 0; bj < 2; ++bj) {
;                     const int c = u.pn * 256 + bj * 128 + wc * 32 + fq * 8; const int g32 = u.pn * 8 + bj * 4 + wc;
;                     f32x4 v0 = acc[ai][bj][m][0] * rs, v1 = acc[ai][bj][m][1] * rs;
;                     if ((g32 % 3) == 2) {
;                         const int ib = 8 * (fq & 1);
;                         const f32x4 c0 = *(const f32x4*)(COS + (size_t)row * 16 + ib), c1 = *(const f32x4*)(COS + (size_t)row * 16 + ib + 4);
;                         const f32x4 s0 = *(const f32x4*)(SIN + (size_t)row * 16 + ib), s1 = *(const f32x4*)(SIN + (size_t)row * 16 + ib + 4);
;                         f32x4 p0, p1;
; #pragma unroll
;                         for (int i = 0; i < 4; ++i) { p0[i] = xor32(v0[i]); p1[i] = xor32(v1[i]); }
;                         const float sg = (fq < 2) ? -1.f : 1.f;
;                         v0 = v0 * c0 + p0 * s0 * sg; v1 = v1 * c1 + p1 * s1 * sg;
;                     }
;                     *(u32x4*)(QM + (size_t)row * 768 + c) = pack8(v0, v1);
.LBB0_656:
	s_and_b32 s7, s60, 0x100
	v_mov_b32_e32 v0, v188
	s_lshl_b32 s7, s7, 3
	s_add_i32 s7, s7, 0
	v_and_or_b32 v152, v0, 15, s56
	v_bfe_u32 v134, v0, 4, 2
	v_lshl_add_u32 v0, v152, 3, s7
	s_lshl_b32 s7, s6, 3
	s_or_b32 s7, s7, s55
	v_add_u32_e32 v151, 0x22400, v0
	ds_read_b32 v138, v151
	s_mul_hi_i32 s12, s7, 0x55555556
	s_lshl_b32 s3, s3, 8
	s_lshr_b32 s13, s12, 31
	v_add_u32_e32 v136, s3, v152
	s_add_i32 s12, s12, s13
	v_lshlrev_b32_e32 v153, 3, v134
	v_ashrrev_i32_e32 v137, 31, v136
	s_mul_i32 s12, s12, 3
	v_and_b32_e32 v139, 8, v153
	v_cmp_gt_u32_e32 vcc, 2, v134
	v_lshlrev_b64 v[154:155], 4, v[136:137]
	s_sub_i32 s12, s7, s12
	v_cndmask_b32_e64 v134, 1.0, -1.0, vcc
	s_waitcnt lgkmcnt(0)
	v_pk_mul_f32 v[146:147], v[122:123], v[138:139] op_sel_hi:[1,0]
	s_cmp_eq_u32 s12, 2
	v_lshlrev_b64 v[122:123], 2, v[154:155]
	v_mov_b32_e32 v135, v134
	v_pk_mul_f32 v[140:141], v[128:129], v[138:139] op_sel_hi:[1,0]
	v_pk_mul_f32 v[142:143], v[126:127], v[138:139] op_sel_hi:[1,0]
	v_pk_mul_f32 v[144:145], v[124:125], v[138:139] op_sel_hi:[1,0]
	s_cselect_b64 s[14:15], -1, 0
	s_cmp_lg_u32 s12, 2
	v_lshl_add_u64 v[128:129], s[26:27], 0, v[122:123]
	v_lshlrev_b32_e32 v0, 2, v139
	v_lshl_add_u64 v[126:127], s[28:29], 0, v[122:123]
	s_cmp_eq_u32 s12, 0
	s_cbranch_scc1 .Luq_nopf
	v_lshl_add_u64 v[240:241], v[128:129], 0, v[0:1]
	v_lshl_add_u64 v[242:243], v[126:127], 0, v[0:1]
	global_load_dwordx4 v[194:197], v[240:241], off
	global_load_dwordx4 v[198:201], v[240:241], off offset:16
	global_load_dwordx4 v[202:205], v[242:243], off
	global_load_dwordx4 v[206:209], v[242:243], off offset:16
	global_load_dwordx4 v[214:217], v[240:241], off offset:1024
	global_load_dwordx4 v[218:221], v[240:241], off offset:1040
	global_load_dwordx4 v[222:225], v[242:243], off offset:1024
	global_load_dwordx4 v[226:229], v[242:243], off offset:1040
	global_load_dwordx4 v[176:179], v[240:241], off offset:2048
	global_load_dwordx4 v[180:183], v[240:241], off offset:2064
	global_load_dwordx4 v[184:187], v[242:243], off offset:2048
	global_load_dwordx4 v[230:233], v[242:243], off offset:2064
	s_mov_b64 s[100:101], 0x2000
	v_lshl_add_u64 v[244:245], v[240:241], 0, s[100:101]
	v_lshl_add_u64 v[246:247], v[242:243], 0, s[100:101]
.Luq_nopf:
	s_cmp_lg_u32 s12, 2
	s_cbranch_scc1 .LBB0_658
	v_lshl_add_u64 v[122:123], v[128:129], 0, v[0:1]
	v_lshl_add_u64 v[162:163], v[126:127], 0, v[0:1]
	s_waitcnt vmcnt(8)
	v_mov_b32_e32 v154, v194
	v_mov_b32_e32 v155, v195
	v_mov_b32_e32 v156, v196
	v_mov_b32_e32 v157, v197
	v_mov_b32_e32 v122, v198
	v_mov_b32_e32 v123, v199
	v_mov_b32_e32 v124, v200
	v_mov_b32_e32 v125, v201
	v_mov_b32_e32 v158, v202
	v_mov_b32_e32 v159, v203
	v_mov_b32_e32 v160, v204
	v_mov_b32_e32 v161, v205
	v_mov_b32_e32 v162, v206
	v_mov_b32_e32 v163, v207
	v_mov_b32_e32 v164, v208
	v_mov_b32_e32 v165, v209
	global_load_dwordx4 v[194:197], v[240:241], off offset:3072
	global_load_dwordx4 v[198:201], v[240:241], off offset:3088
	global_load_dwordx4 v[202:205], v[242:243], off offset:3072
	global_load_dwordx4 v[206:209], v[242:243], off offset:3088
	v_mov_b32_e32 v137, v142
	v_mov_b32_e32 v139, v142
	s_nop 1
	v_permlane32_swap_b32_e32 v137, v139
	v_cndmask_b32_e64 v166, v137, v139, s[4:5]
	v_mov_b32_e32 v137, v146
	v_mov_b32_e32 v139, v146
	s_nop 1
	v_permlane32_swap_b32_e32 v137, v139
	v_cndmask_b32_e64 v168, v137, v139, s[4:5]
	v_mov_b32_e32 v137, v143
	v_mov_b32_e32 v139, v143
	s_nop 1
	v_permlane32_swap_b32_e32 v137, v139
	v_cndmask_b32_e64 v167, v137, v139, s[4:5]
	v_mov_b32_e32 v137, v147
	v_mov_b32_e32 v139, v147
	s_nop 1
	v_permlane32_swap_b32_e32 v137, v139
	v_cndmask_b32_e64 v169, v137, v139, s[4:5]
	v_mov_b32_e32 v137, v140
	v_mov_b32_e32 v139, v140
	s_nop 1
	v_permlane32_swap_b32_e32 v137, v139
	v_cndmask_b32_e64 v170, v137, v139, s[4:5]
	v_mov_b32_e32 v137, v144
	v_mov_b32_e32 v139, v144
	s_nop 1
	v_permlane32_swap_b32_e32 v137, v139
	v_cndmask_b32_e64 v172, v137, v139, s[4:5]
	v_mov_b32_e32 v137, v141
	v_mov_b32_e32 v139, v141
	s_nop 1
	v_permlane32_swap_b32_e32 v137, v139
	v_cndmask_b32_e64 v171, v137, v139, s[4:5]
	v_mov_b32_e32 v137, v145
	v_mov_b32_e32 v139, v145
	s_nop 1
	v_permlane32_swap_b32_e32 v137, v139
	v_cndmask_b32_e64 v173, v137, v139, s[4:5]
	s_waitcnt lgkmcnt(0)
	v_pk_mul_f32 v[160:161], v[160:161], v[170:171]
	v_pk_mul_f32 v[158:159], v[158:159], v[166:167]
	v_mov_b32_e32 v166, v134
	v_mov_b32_e32 v167, v134
	v_pk_mul_f32 v[158:159], v[134:135], v[158:159]
	v_pk_mul_f32 v[160:161], v[166:167], v[160:161]
	v_pk_fma_f32 v[142:143], v[142:143], v[154:155], v[158:159]
	v_pk_fma_f32 v[140:141], v[140:141], v[156:157], v[160:161]
	v_pk_mul_f32 v[154:155], v[164:165], v[172:173]
	v_pk_mul_f32 v[156:157], v[162:163], v[168:169]
	v_pk_mul_f32 v[154:155], v[166:167], v[154:155]
	v_pk_mul_f32 v[156:157], v[134:135], v[156:157]
	v_pk_fma_f32 v[144:145], v[144:145], v[124:125], v[154:155]
	v_pk_fma_f32 v[146:147], v[146:147], v[122:123], v[156:157]
; __device__ __forceinline__ float xor32(float x) { auto rr = __builtin_amdgcn_permlane32_swap(__float_as_uint(x), __float_as_uint(x), false, false); return __uint_as_float(((unsigned)(threadIdx.x & 32)) ? rr[0] : rr[1]); }
; __device__ __forceinline__ u32x4 pack8(f32x4 a, f32x4 b) { u32x4 w; w.x = pk2(a[0], a[1]); w.y = pk2(a[2], a[3]); w.z = pk2(b[0], b[1]); w.w = pk2(b[2], b[3]); return w; }
;     __device__ __forceinline__ void operator()(const f32x4 (&acc)[2][2][4][2], const Unit& u, int ui, int wr, int wc, int fr, int fq, LAS unsigned char* lds) const {
;     ...
;                 for (int bj = 0; bj < 2; ++bj) {
;                     const int c = u.pn * 256 + bj * 128 + wc * 32 + fq * 8; const int g32 = u.pn * 8 + bj * 4 + wc;
;                     f32x4 v0 = acc[ai][bj][m][0] * rs, v1 = acc[ai][bj][m][1] * rs;
;                     if ((g32 % 3) == 2) {
;                         const int ib = 8 * (fq & 1);
;                         const f32x4 c0 = *(const f32x4*)(COS + (size_t)row * 16 + ib), c1 = *(const f32x4*)(COS + (size_t)row * 16 + ib + 4);
;                         const f32x4 s0 = *(const f32x4*)(SIN + (size_t)row * 16 + ib), s1 = *(const f32x4*)(SIN + (size_t)row * 16 + ib + 4);
;                         f32x4 p0, p1;
; #pragma unroll
;                         for (int i = 0; i < 4; ++i) { p0[i] = xor32(v0[i]); p1[i] = xor32(v1[i]); }
;                         const float sg = (fq < 2) ? -1.f : 1.f;
;                         v0 = v0 * c0 + p0 * s0 * sg; v1 = v1 * c1 + p1 * s1 * sg;
;                     }
;                     *(u32x4*)(QM + (size_t)row * 768 + c) = pack8(v0, v1);
.LBB0_658:
	s_lshl_b32 s6, s6, 8
	s_or_b32 s6, s6, s57
	v_or_b32_e32 v122, s6, v153
	v_mov_b64_e32 v[124:125], s[22:23]
	s_movk_i32 s6, 0x600
	v_mad_i64_i32 v[124:125], s[12:13], v136, s6, v[124:125]
	s_or_b32 s6, s7, 4
	s_mul_hi_i32 s7, s6, 0x55555556
	s_lshr_b32 s12, s7, 31
	s_add_i32 s7, s7, s12
	s_mul_i32 s7, s7, 3
	s_sub_i32 s6, s6, s7
	v_mov_b32_e32 v139, v138
	v_cvt_pk_bf16_f32 v155, v140, v141
	v_ashrrev_i32_e32 v123, 31, v122
	v_mov_b32_e32 v140, v138
	v_mov_b32_e32 v141, v138
	s_cmp_eq_u32 s6, 2
	v_readlane_b32 s65, v255, 25
	v_mov_b64_e32 v[248:249], v[210:211]
	v_mov_b32_e32 v234, v189
	v_mov_b32_e32 v235, v212
	v_mov_b32_e32 v236, v213
	v_mov_b64_e32 v[238:239], v[148:149]
	v_cvt_pk_bf16_f32 v154, v142, v143
	v_cvt_pk_bf16_f32 v156, v146, v147
	v_cvt_pk_bf16_f32 v157, v144, v145
	v_lshl_add_u64 v[124:125], v[122:123], 1, v[124:125]
	v_pk_mul_f32 v[120:121], v[120:121], v[140:141]
	v_pk_mul_f32 v[118:119], v[118:119], v[138:139]
	v_pk_mul_f32 v[140:141], v[116:117], v[140:141]
	s_cselect_b64 s[48:49], -1, 0
	s_cmp_lg_u32 s6, 2
	v_pk_mul_f32 v[138:139], v[114:115], v[138:139]
	global_store_dwordx4 v[124:125], v[154:157], off
	s_cbranch_scc1 .LBB0_660
	v_lshl_add_u64 v[114:115], v[128:129], 0, v[0:1]
	v_lshl_add_u64 v[146:147], v[126:127], 0, v[0:1]
	s_waitcnt vmcnt(8)
	v_mov_b32_e32 v142, v194
	v_mov_b32_e32 v143, v195
	v_mov_b32_e32 v144, v196
	v_mov_b32_e32 v145, v197
	v_mov_b32_e32 v114, v198
	v_mov_b32_e32 v115, v199
	v_mov_b32_e32 v116, v200
	v_mov_b32_e32 v117, v201
	v_mov_b32_e32 v126, v202
	v_mov_b32_e32 v127, v203
	v_mov_b32_e32 v128, v204
	v_mov_b32_e32 v129, v205
	v_mov_b32_e32 v154, v206
	v_mov_b32_e32 v155, v207
	v_mov_b32_e32 v156, v208
	v_mov_b32_e32 v157, v209
	global_load_dwordx4 v[194:197], v[240:241], off offset:3072
	global_load_dwordx4 v[198:201], v[240:241], off offset:3088
	global_load_dwordx4 v[202:205], v[242:243], off offset:3072
	global_load_dwordx4 v[206:209], v[242:243], off offset:3088
	v_mov_b32_e32 v137, v118
	v_mov_b32_e32 v146, v118
	s_nop 1
	v_permlane32_swap_b32_e32 v137, v146
	v_cndmask_b32_e64 v146, v137, v146, s[4:5]
	v_mov_b32_e32 v137, v138
	v_mov_b32_e32 v147, v138
	s_nop 1
	v_permlane32_swap_b32_e32 v137, v147
	v_cndmask_b32_e64 v158, v137, v147, s[4:5]
	v_mov_b32_e32 v137, v119
	v_mov_b32_e32 v147, v119
	s_nop 1
	v_permlane32_swap_b32_e32 v137, v147
	v_cndmask_b32_e64 v147, v137, v147, s[4:5]
	v_mov_b32_e32 v137, v139
	v_mov_b32_e32 v153, v139
	s_nop 1
	v_permlane32_swap_b32_e32 v137, v153
	v_cndmask_b32_e64 v159, v137, v153, s[4:5]
	v_mov_b32_e32 v137, v120
	v_mov_b32_e32 v153, v120
	s_nop 1
	v_permlane32_swap_b32_e32 v137, v153
	v_cndmask_b32_e64 v160, v137, v153, s[4:5]
	v_mov_b32_e32 v137, v140
	v_mov_b32_e32 v153, v140
	s_nop 1
	v_permlane32_swap_b32_e32 v137, v153
	v_cndmask_b32_e64 v162, v137, v153, s[4:5]
	v_mov_b32_e32 v137, v121
	v_mov_b32_e32 v153, v121
	s_nop 1
	v_permlane32_swap_b32_e32 v137, v153
	v_cndmask_b32_e64 v161, v137, v153, s[4:5]
	v_mov_b32_e32 v137, v141
	v_mov_b32_e32 v153, v141
	s_nop 1
	v_permlane32_swap_b32_e32 v137, v153
	v_cndmask_b32_e64 v163, v137, v153, s[4:5]
	s_waitcnt lgkmcnt(0)
	v_pk_mul_f32 v[128:129], v[128:129], v[160:161]
	v_pk_mul_f32 v[126:127], v[126:127], v[146:147]
	v_mov_b32_e32 v146, v134
	v_mov_b32_e32 v147, v134
	v_pk_mul_f32 v[126:127], v[134:135], v[126:127]
	v_pk_mul_f32 v[128:129], v[146:147], v[128:129]
	v_pk_fma_f32 v[118:119], v[118:119], v[142:143], v[126:127]
	v_pk_fma_f32 v[120:121], v[120:121], v[144:145], v[128:129]
	v_pk_mul_f32 v[126:127], v[156:157], v[162:163]
	v_pk_mul_f32 v[128:129], v[154:155], v[158:159]
	v_pk_mul_f32 v[126:127], v[146:147], v[126:127]
	v_pk_mul_f32 v[128:129], v[134:135], v[128:129]
	v_pk_fma_f32 v[140:141], v[140:141], v[116:117], v[126:127]
	v_pk_fma_f32 v[138:139], v[138:139], v[114:115], v[128:129]
.LBB0_660:
	v_cvt_pk_bf16_f32 v114, v118, v119
	v_cvt_pk_bf16_f32 v115, v120, v121
	v_cvt_pk_bf16_f32 v116, v138, v139
	v_cvt_pk_bf16_f32 v117, v140, v141
	global_store_dwordx4 v[124:125], v[114:117], off offset:256
	ds_read_b32 v114, v151 offset:128
	s_andn2_b64 vcc, exec, s[14:15]
	v_add3_u32 v116, s3, v152, 16
	v_ashrrev_i32_e32 v117, 31, v116
	v_lshlrev_b64 v[128:129], 4, v[116:117]
	s_waitcnt lgkmcnt(0)
	v_pk_mul_f32 v[126:127], v[106:107], v[114:115] op_sel_hi:[1,0]
	v_cndmask_b32_e64 v106, 0, 1, s[14:15]
	v_cmp_ne_u32_e64 s[12:13], 1, v106
	v_lshlrev_b64 v[106:107], 2, v[128:129]
	v_pk_mul_f32 v[118:119], v[112:113], v[114:115] op_sel_hi:[1,0]
	v_pk_mul_f32 v[120:121], v[110:111], v[114:115] op_sel_hi:[1,0]
	v_pk_mul_f32 v[124:125], v[108:109], v[114:115] op_sel_hi:[1,0]
	v_lshl_add_u64 v[112:113], s[26:27], 0, v[106:107]
	v_lshl_add_u64 v[110:111], s[28:29], 0, v[106:107]
	s_cbranch_vccnz .LBB0_662
; __device__ __forceinline__ float xor32(float x) { auto rr = __builtin_amdgcn_permlane32_swap(__float_as_uint(x), __float_as_uint(x), false, false); return __uint_as_float(((unsigned)(threadIdx.x & 32)) ? rr[0] : rr[1]); }
; __device__ __forceinline__ u32x4 pack8(f32x4 a, f32x4 b) { u32x4 w; w.x = pk2(a[0], a[1]); w.y = pk2(a[2], a[3]); w.z = pk2(b[0], b[1]); w.w = pk2(b[2], b[3]); return w; }
;     __device__ __forceinline__ void operator()(const f32x4 (&acc)[2][2][4][2], const Unit& u, int ui, int wr, int wc, int fr, int fq, LAS unsigned char* lds) const {
;     ...
;                 for (int bj = 0; bj < 2; ++bj) {
;                     const int c = u.pn * 256 + bj * 128 + wc * 32 + fq * 8; const int g32 = u.pn * 8 + bj * 4 + wc;
;                     f32x4 v0 = acc[ai][bj][m][0] * rs, v1 = acc[ai][bj][m][1] * rs;
;                     if ((g32 % 3) == 2) {
;                         const int ib = 8 * (fq & 1);
;                         const f32x4 c0 = *(const f32x4*)(COS + (size_t)row * 16 + ib), c1 = *(const f32x4*)(COS + (size_t)row * 16 + ib + 4);
;                         const f32x4 s0 = *(const f32x4*)(SIN + (size_t)row * 16 + ib), s1 = *(const f32x4*)(SIN + (size_t)row * 16 + ib + 4);
;                         f32x4 p0, p1;
; #pragma unroll
;                         for (int i = 0; i < 4; ++i) { p0[i] = xor32(v0[i]); p1[i] = xor32(v1[i]); }
;                         const float sg = (fq < 2) ? -1.f : 1.f;
;                         v0 = v0 * c0 + p0 * s0 * sg; v1 = v1 * c1 + p1 * s1 * sg;
;                     }
;                     *(u32x4*)(QM + (size_t)row * 768 + c) = pack8(v0, v1);
	v_lshl_add_u64 v[106:107], v[112:113], 0, v[0:1]
	v_lshl_add_u64 v[128:129], v[110:111], 0, v[0:1]
	s_waitcnt vmcnt(10)
	v_mov_b32_e32 v138, v214
	v_mov_b32_e32 v139, v215
	v_mov_b32_e32 v140, v216
	v_mov_b32_e32 v141, v217
	v_mov_b32_e32 v106, v218
	v_mov_b32_e32 v107, v219
	v_mov_b32_e32 v108, v220
	v_mov_b32_e32 v109, v221
	v_mov_b32_e32 v142, v222
	v_mov_b32_e32 v143, v223
	v_mov_b32_e32 v144, v224
	v_mov_b32_e32 v145, v225
	v_mov_b32_e32 v154, v226
	v_mov_b32_e32 v155, v227
	v_mov_b32_e32 v156, v228
	v_mov_b32_e32 v157, v229
	global_load_dwordx4 v[214:217], v[244:245], off
	global_load_dwordx4 v[218:221], v[244:245], off offset:16
	global_load_dwordx4 v[222:225], v[246:247], off
	global_load_dwordx4 v[226:229], v[246:247], off offset:16
	v_mov_b32_e32 v115, v120
	v_mov_b32_e32 v117, v120
	s_nop 1
	v_permlane32_swap_b32_e32 v115, v117
	v_cndmask_b32_e64 v128, v115, v117, s[4:5]
	v_mov_b32_e32 v115, v126
	v_mov_b32_e32 v117, v126
	s_nop 1
	v_permlane32_swap_b32_e32 v115, v117
	v_cndmask_b32_e64 v146, v115, v117, s[4:5]
	v_mov_b32_e32 v115, v121
	v_mov_b32_e32 v117, v121
	s_nop 1
	v_permlane32_swap_b32_e32 v115, v117
	v_cndmask_b32_e64 v129, v115, v117, s[4:5]
	v_mov_b32_e32 v115, v127
	v_mov_b32_e32 v117, v127
	s_nop 1
	v_permlane32_swap_b32_e32 v115, v117
	v_cndmask_b32_e64 v147, v115, v117, s[4:5]
	v_mov_b32_e32 v115, v118
	v_mov_b32_e32 v117, v118
	s_nop 1
	v_permlane32_swap_b32_e32 v115, v117
	v_cndmask_b32_e64 v158, v115, v117, s[4:5]
	v_mov_b32_e32 v115, v124
	v_mov_b32_e32 v117, v124
	s_nop 1
	v_permlane32_swap_b32_e32 v115, v117
	v_cndmask_b32_e64 v160, v115, v117, s[4:5]
	v_mov_b32_e32 v115, v119
	v_mov_b32_e32 v117, v119
	s_nop 1
	v_permlane32_swap_b32_e32 v115, v117
	v_cndmask_b32_e64 v159, v115, v117, s[4:5]
	v_mov_b32_e32 v115, v125
	v_mov_b32_e32 v117, v125
	s_nop 1
	v_permlane32_swap_b32_e32 v115, v117
	v_cndmask_b32_e64 v161, v115, v117, s[4:5]
	s_waitcnt lgkmcnt(0)
	v_pk_mul_f32 v[128:129], v[142:143], v[128:129]
	s_nop 0
	v_pk_mul_f32 v[128:129], v[134:135], v[128:129]
	v_pk_mul_f32 v[144:145], v[144:145], v[158:159]
	v_mov_b32_e32 v142, v134
	v_mov_b32_e32 v143, v134
	v_pk_fma_f32 v[120:121], v[120:121], v[138:139], v[128:129]
	v_pk_mul_f32 v[128:129], v[156:157], v[160:161]
	v_pk_mul_f32 v[138:139], v[154:155], v[146:147]
	v_pk_mul_f32 v[144:145], v[142:143], v[144:145]
	v_pk_mul_f32 v[138:139], v[134:135], v[138:139]
	v_pk_mul_f32 v[128:129], v[142:143], v[128:129]
	v_pk_fma_f32 v[118:119], v[118:119], v[140:141], v[144:145]
	v_pk_fma_f32 v[124:125], v[124:125], v[108:109], v[128:129]
	v_pk_fma_f32 v[126:127], v[126:127], v[106:107], v[138:139]
.LBB0_662:
	v_mov_b64_e32 v[106:107], s[22:23]
	s_movk_i32 s6, 0x600
	v_mov_b32_e32 v108, v114
	v_mov_b32_e32 v109, v114
	v_mov_b32_e32 v115, v114
	v_mad_i64_i32 v[106:107], s[6:7], v116, s6, v[106:107]
	v_pk_mul_f32 v[104:105], v[104:105], v[108:109]
	v_pk_mul_f32 v[108:109], v[100:101], v[108:109]
	v_cndmask_b32_e64 v100, 0, 1, s[48:49]
	v_cvt_pk_bf16_f32 v138, v120, v121
	v_cvt_pk_bf16_f32 v139, v118, v119
	v_cvt_pk_bf16_f32 v140, v126, v127
	v_cvt_pk_bf16_f32 v141, v124, v125
	v_lshl_add_u64 v[106:107], v[122:123], 1, v[106:107]
	v_pk_mul_f32 v[102:103], v[102:103], v[114:115]
	v_cmp_ne_u32_e64 s[14:15], 1, v100
	s_andn2_b64 vcc, exec, s[48:49]
	v_pk_mul_f32 v[114:115], v[98:99], v[114:115]
	global_store_dwordx4 v[106:107], v[138:141], off
	s_cbranch_vccnz .LBB0_664
	v_lshl_add_u64 v[98:99], v[112:113], 0, v[0:1]
	v_lshl_add_u64 v[120:121], v[110:111], 0, v[0:1]
	s_waitcnt vmcnt(10)
	v_mov_b32_e32 v116, v214
	v_mov_b32_e32 v117, v215
	v_mov_b32_e32 v118, v216
	v_mov_b32_e32 v119, v217
	v_mov_b32_e32 v98, v218
	v_mov_b32_e32 v99, v219
	v_mov_b32_e32 v100, v220
	v_mov_b32_e32 v101, v221
	v_mov_b32_e32 v110, v222
	v_mov_b32_e32 v111, v223
	v_mov_b32_e32 v112, v224
	v_mov_b32_e32 v113, v225
	v_mov_b32_e32 v124, v226
	v_mov_b32_e32 v125, v227
	v_mov_b32_e32 v126, v228
	v_mov_b32_e32 v127, v229
	global_load_dwordx4 v[214:217], v[244:245], off
	global_load_dwordx4 v[218:221], v[244:245], off offset:16
	global_load_dwordx4 v[222:225], v[246:247], off
	global_load_dwordx4 v[226:229], v[246:247], off offset:16
	v_mov_b32_e32 v120, v102
	v_mov_b32_e32 v121, v102
	s_nop 1
	v_permlane32_swap_b32_e32 v120, v121
	v_cndmask_b32_e64 v120, v120, v121, s[4:5]
	v_mov_b32_e32 v121, v114
	v_mov_b32_e32 v128, v114
	s_nop 1
	v_permlane32_swap_b32_e32 v121, v128
	v_cndmask_b32_e64 v128, v121, v128, s[4:5]
	v_mov_b32_e32 v121, v103
	v_mov_b32_e32 v129, v103
	s_nop 1
	v_permlane32_swap_b32_e32 v121, v129
	v_cndmask_b32_e64 v121, v121, v129, s[4:5]
	v_mov_b32_e32 v129, v115
	v_mov_b32_e32 v137, v115
	s_nop 1
	v_permlane32_swap_b32_e32 v129, v137
	v_cndmask_b32_e64 v129, v129, v137, s[4:5]
	v_mov_b32_e32 v137, v104
	v_mov_b32_e32 v138, v104
	s_nop 1
	v_permlane32_swap_b32_e32 v137, v138
	v_cndmask_b32_e64 v138, v137, v138, s[4:5]
	v_mov_b32_e32 v137, v108
	v_mov_b32_e32 v139, v108
	s_nop 1
	v_permlane32_swap_b32_e32 v137, v139
	v_cndmask_b32_e64 v140, v137, v139, s[4:5]
	v_mov_b32_e32 v137, v105
	v_mov_b32_e32 v139, v105
	s_nop 1
	v_permlane32_swap_b32_e32 v137, v139
	v_cndmask_b32_e64 v139, v137, v139, s[4:5]
	v_mov_b32_e32 v137, v109
	v_mov_b32_e32 v141, v109
	s_nop 1
	v_permlane32_swap_b32_e32 v137, v141
	v_cndmask_b32_e64 v141, v137, v141, s[4:5]
	s_waitcnt lgkmcnt(0)
	v_pk_mul_f32 v[112:113], v[112:113], v[138:139]
	v_pk_mul_f32 v[110:111], v[110:111], v[120:121]
	v_mov_b32_e32 v120, v134
	v_mov_b32_e32 v121, v134
	v_pk_mul_f32 v[110:111], v[134:135], v[110:111]
	v_pk_mul_f32 v[112:113], v[120:121], v[112:113]
	v_pk_fma_f32 v[102:103], v[102:103], v[116:117], v[110:111]
	v_pk_fma_f32 v[104:105], v[104:105], v[118:119], v[112:113]
	v_pk_mul_f32 v[110:111], v[126:127], v[140:141]
	v_pk_mul_f32 v[112:113], v[124:125], v[128:129]
	v_pk_mul_f32 v[110:111], v[120:121], v[110:111]
	v_pk_mul_f32 v[112:113], v[134:135], v[112:113]
	v_pk_fma_f32 v[108:109], v[108:109], v[100:101], v[110:111]
	v_pk_fma_f32 v[114:115], v[114:115], v[98:99], v[112:113]
; __device__ __forceinline__ float xor32(float x) { auto rr = __builtin_amdgcn_permlane32_swap(__float_as_uint(x), __float_as_uint(x), false, false); return __uint_as_float(((unsigned)(threadIdx.x & 32)) ? rr[0] : rr[1]); }
; __device__ __forceinline__ u32x4 pack8(f32x4 a, f32x4 b) { u32x4 w; w.x = pk2(a[0], a[1]); w.y = pk2(a[2], a[3]); w.z = pk2(b[0], b[1]); w.w = pk2(b[2], b[3]); return w; }
;     __device__ __forceinline__ void operator()(const f32x4 (&acc)[2][2][4][2], const Unit& u, int ui, int wr, int wc, int fr, int fq, LAS unsigned char* lds) const {
;     ...
;                 for (int bj = 0; bj < 2; ++bj) {
;                     const int c = u.pn * 256 + bj * 128 + wc * 32 + fq * 8; const int g32 = u.pn * 8 + bj * 4 + wc;
;                     f32x4 v0 = acc[ai][bj][m][0] * rs, v1 = acc[ai][bj][m][1] * rs;
;                     if ((g32 % 3) == 2) {
;                         const int ib = 8 * (fq & 1);
;                         const f32x4 c0 = *(const f32x4*)(COS + (size_t)row * 16 + ib), c1 = *(const f32x4*)(COS + (size_t)row * 16 + ib + 4);
;                         const f32x4 s0 = *(const f32x4*)(SIN + (size_t)row * 16 + ib), s1 = *(const f32x4*)(SIN + (size_t)row * 16 + ib + 4);
;                         f32x4 p0, p1;
; #pragma unroll
;                         for (int i = 0; i < 4; ++i) { p0[i] = xor32(v0[i]); p1[i] = xor32(v1[i]); }
;                         const float sg = (fq < 2) ? -1.f : 1.f;
;                         v0 = v0 * c0 + p0 * s0 * sg; v1 = v1 * c1 + p1 * s1 * sg;
;                     }
;                     *(u32x4*)(QM + (size_t)row * 768 + c) = pack8(v0, v1);
.LBB0_664:
	v_cvt_pk_bf16_f32 v98, v102, v103
	v_cvt_pk_bf16_f32 v99, v104, v105
	v_cvt_pk_bf16_f32 v100, v114, v115
	v_cvt_pk_bf16_f32 v101, v108, v109
	global_store_dwordx4 v[106:107], v[98:101], off offset:256
	ds_read_b32 v98, v151 offset:256
	s_and_b64 vcc, exec, s[12:13]
	v_add3_u32 v100, s3, v152, 32
	v_ashrrev_i32_e32 v101, 31, v100
	v_lshlrev_b64 v[110:111], 4, v[100:101]
	s_waitcnt lgkmcnt(0)
	v_pk_mul_f32 v[108:109], v[90:91], v[98:99] op_sel_hi:[1,0]
	v_lshlrev_b64 v[90:91], 2, v[110:111]
	v_pk_mul_f32 v[102:103], v[96:97], v[98:99] op_sel_hi:[1,0]
	v_pk_mul_f32 v[104:105], v[94:95], v[98:99] op_sel_hi:[1,0]
	v_pk_mul_f32 v[106:107], v[92:93], v[98:99] op_sel_hi:[1,0]
	v_lshl_add_u64 v[96:97], s[26:27], 0, v[90:91]
	v_lshl_add_u64 v[94:95], s[28:29], 0, v[90:91]
	s_cbranch_vccnz .LBB0_666
	v_lshl_add_u64 v[90:91], v[96:97], 0, v[0:1]
	v_lshl_add_u64 v[118:119], v[94:95], 0, v[0:1]
	s_waitcnt vmcnt(12)
	v_mov_b32_e32 v110, v176
	v_mov_b32_e32 v111, v177
	v_mov_b32_e32 v112, v178
	v_mov_b32_e32 v113, v179
	v_mov_b32_e32 v90, v180
	v_mov_b32_e32 v91, v181
	v_mov_b32_e32 v92, v182
	v_mov_b32_e32 v93, v183
	v_mov_b32_e32 v114, v184
	v_mov_b32_e32 v115, v185
	v_mov_b32_e32 v116, v186
	v_mov_b32_e32 v117, v187
	v_mov_b32_e32 v118, v230
	v_mov_b32_e32 v119, v231
	v_mov_b32_e32 v120, v232
	v_mov_b32_e32 v121, v233
	global_load_dwordx4 v[176:179], v[244:245], off offset:1024
	global_load_dwordx4 v[180:183], v[244:245], off offset:1040
	global_load_dwordx4 v[184:187], v[246:247], off offset:1024
	global_load_dwordx4 v[230:233], v[246:247], off offset:1040
	v_mov_b32_e32 v99, v104
	v_mov_b32_e32 v101, v104
	s_nop 1
	v_permlane32_swap_b32_e32 v99, v101
	v_cndmask_b32_e64 v124, v99, v101, s[4:5]
	v_mov_b32_e32 v99, v108
	v_mov_b32_e32 v101, v108
	s_nop 1
	v_permlane32_swap_b32_e32 v99, v101
	v_cndmask_b32_e64 v126, v99, v101, s[4:5]
	v_mov_b32_e32 v99, v105
	v_mov_b32_e32 v101, v105
	s_nop 1
	v_permlane32_swap_b32_e32 v99, v101
	v_cndmask_b32_e64 v125, v99, v101, s[4:5]
	v_mov_b32_e32 v99, v109
	v_mov_b32_e32 v101, v109
	s_nop 1
	v_permlane32_swap_b32_e32 v99, v101
	v_cndmask_b32_e64 v127, v99, v101, s[4:5]
	v_mov_b32_e32 v99, v102
	v_mov_b32_e32 v101, v102
	s_nop 1
	v_permlane32_swap_b32_e32 v99, v101
	v_cndmask_b32_e64 v128, v99, v101, s[4:5]
	v_mov_b32_e32 v99, v106
	v_mov_b32_e32 v101, v106
	s_nop 1
	v_permlane32_swap_b32_e32 v99, v101
	v_cndmask_b32_e64 v138, v99, v101, s[4:5]
	v_mov_b32_e32 v99, v103
	v_mov_b32_e32 v101, v103
	s_nop 1
	v_permlane32_swap_b32_e32 v99, v101
	v_cndmask_b32_e64 v129, v99, v101, s[4:5]
	v_mov_b32_e32 v99, v107
	v_mov_b32_e32 v101, v107
	s_nop 1
	v_permlane32_swap_b32_e32 v99, v101
	v_cndmask_b32_e64 v139, v99, v101, s[4:5]
	s_waitcnt lgkmcnt(0)
	v_pk_mul_f32 v[116:117], v[116:117], v[128:129]
	v_pk_mul_f32 v[114:115], v[114:115], v[124:125]
	v_mov_b32_e32 v124, v134
	v_mov_b32_e32 v125, v134
	v_pk_mul_f32 v[114:115], v[134:135], v[114:115]
	v_pk_mul_f32 v[116:117], v[124:125], v[116:117]
	v_pk_fma_f32 v[104:105], v[104:105], v[110:111], v[114:115]
	v_pk_fma_f32 v[102:103], v[102:103], v[112:113], v[116:117]
	v_pk_mul_f32 v[110:111], v[120:121], v[138:139]
	v_pk_mul_f32 v[112:113], v[118:119], v[126:127]
	v_pk_mul_f32 v[110:111], v[124:125], v[110:111]
	v_pk_mul_f32 v[112:113], v[134:135], v[112:113]
	v_pk_fma_f32 v[106:107], v[106:107], v[92:93], v[110:111]
	v_pk_fma_f32 v[108:109], v[108:109], v[90:91], v[112:113]
.LBB0_666:
	v_mov_b64_e32 v[90:91], s[22:23]
	s_movk_i32 s6, 0x600
	v_mov_b32_e32 v99, v98
	v_mad_i64_i32 v[90:91], s[6:7], v100, s6, v[90:91]
	v_mov_b32_e32 v92, v98
	v_mov_b32_e32 v93, v98
	v_cvt_pk_bf16_f32 v110, v104, v105
	v_cvt_pk_bf16_f32 v111, v102, v103
	v_cvt_pk_bf16_f32 v112, v108, v109
	v_cvt_pk_bf16_f32 v113, v106, v107
	v_lshl_add_u64 v[90:91], v[122:123], 1, v[90:91]
	v_pk_mul_f32 v[88:89], v[88:89], v[92:93]
	v_pk_mul_f32 v[86:87], v[86:87], v[98:99]
	v_pk_mul_f32 v[92:93], v[84:85], v[92:93]
	s_and_b64 vcc, exec, s[14:15]
	v_pk_mul_f32 v[98:99], v[82:83], v[98:99]
	global_store_dwordx4 v[90:91], v[110:113], off
	s_cbranch_vccnz .LBB0_668
	v_lshl_add_u64 v[82:83], v[96:97], 0, v[0:1]
	v_lshl_add_u64 v[104:105], v[94:95], 0, v[0:1]
	s_waitcnt vmcnt(12)
	v_mov_b32_e32 v100, v176
	v_mov_b32_e32 v101, v177
	v_mov_b32_e32 v102, v178
	v_mov_b32_e32 v103, v179
	v_mov_b32_e32 v82, v180
	v_mov_b32_e32 v83, v181
	v_mov_b32_e32 v84, v182
	v_mov_b32_e32 v85, v183
	v_mov_b32_e32 v94, v184
	v_mov_b32_e32 v95, v185
	v_mov_b32_e32 v96, v186
	v_mov_b32_e32 v97, v187
	v_mov_b32_e32 v104, v230
	v_mov_b32_e32 v105, v231
	v_mov_b32_e32 v106, v232
	v_mov_b32_e32 v107, v233
	global_load_dwordx4 v[176:179], v[244:245], off offset:1024
	global_load_dwordx4 v[180:183], v[244:245], off offset:1040
	global_load_dwordx4 v[184:187], v[246:247], off offset:1024
	global_load_dwordx4 v[230:233], v[246:247], off offset:1040
	v_mov_b32_e32 v108, v86
	v_mov_b32_e32 v109, v86
	s_nop 1
	v_permlane32_swap_b32_e32 v108, v109
	v_cndmask_b32_e64 v108, v108, v109, s[4:5]
	v_mov_b32_e32 v109, v98
	v_mov_b32_e32 v110, v98
	s_nop 1
	v_permlane32_swap_b32_e32 v109, v110
	v_cndmask_b32_e64 v110, v109, v110, s[4:5]
	v_mov_b32_e32 v109, v87
	v_mov_b32_e32 v111, v87
	s_nop 1
	v_permlane32_swap_b32_e32 v109, v111
	v_cndmask_b32_e64 v109, v109, v111, s[4:5]
	v_mov_b32_e32 v111, v99
	v_mov_b32_e32 v112, v99
	s_nop 1
	v_permlane32_swap_b32_e32 v111, v112
	v_cndmask_b32_e64 v111, v111, v112, s[4:5]
	v_mov_b32_e32 v112, v88
	v_mov_b32_e32 v113, v88
	s_nop 1
	v_permlane32_swap_b32_e32 v112, v113
	v_cndmask_b32_e64 v112, v112, v113, s[4:5]
	v_mov_b32_e32 v113, v92
	v_mov_b32_e32 v114, v92
	s_nop 1
	v_permlane32_swap_b32_e32 v113, v114
	v_cndmask_b32_e64 v114, v113, v114, s[4:5]
	v_mov_b32_e32 v113, v89
	v_mov_b32_e32 v115, v89
	s_nop 1
	v_permlane32_swap_b32_e32 v113, v115
	v_cndmask_b32_e64 v113, v113, v115, s[4:5]
	v_mov_b32_e32 v115, v93
	v_mov_b32_e32 v116, v93
	s_nop 1
	v_permlane32_swap_b32_e32 v115, v116
	v_cndmask_b32_e64 v115, v115, v116, s[4:5]
	s_waitcnt lgkmcnt(0)
	v_pk_mul_f32 v[96:97], v[96:97], v[112:113]
	v_pk_mul_f32 v[94:95], v[94:95], v[108:109]
	v_mov_b32_e32 v108, v134
	v_mov_b32_e32 v109, v134
	v_pk_mul_f32 v[94:95], v[134:135], v[94:95]
	v_pk_mul_f32 v[96:97], v[108:109], v[96:97]
	v_pk_fma_f32 v[86:87], v[86:87], v[100:101], v[94:95]
	v_pk_fma_f32 v[88:89], v[88:89], v[102:103], v[96:97]
	v_pk_mul_f32 v[94:95], v[106:107], v[114:115]
	v_pk_mul_f32 v[96:97], v[104:105], v[110:111]
	v_pk_mul_f32 v[94:95], v[108:109], v[94:95]
	v_pk_mul_f32 v[96:97], v[134:135], v[96:97]
	v_pk_fma_f32 v[92:93], v[92:93], v[84:85], v[94:95]
	v_pk_fma_f32 v[98:99], v[98:99], v[82:83], v[96:97]
; __device__ __forceinline__ float xor32(float x) { auto rr = __builtin_amdgcn_permlane32_swap(__float_as_uint(x), __float_as_uint(x), false, false); return __uint_as_float(((unsigned)(threadIdx.x & 32)) ? rr[0] : rr[1]); }
; __device__ __forceinline__ u32x4 pack8(f32x4 a, f32x4 b) { u32x4 w; w.x = pk2(a[0], a[1]); w.y = pk2(a[2], a[3]); w.z = pk2(b[0], b[1]); w.w = pk2(b[2], b[3]); return w; }
;     __device__ __forceinline__ void operator()(const f32x4 (&acc)[2][2][4][2], const Unit& u, int ui, int wr, int wc, int fr, int fq, LAS unsigned char* lds) const {
;     ...
;                 for (int bj = 0; bj < 2; ++bj) {
;                     const int c = u.pn * 256 + bj * 128 + wc * 32 + fq * 8; const int g32 = u.pn * 8 + bj * 4 + wc;
;                     f32x4 v0 = acc[ai][bj][m][0] * rs, v1 = acc[ai][bj][m][1] * rs;
;                     if ((g32 % 3) == 2) {
;                         const int ib = 8 * (fq & 1);
;                         const f32x4 c0 = *(const f32x4*)(COS + (size_t)row * 16 + ib), c1 = *(const f32x4*)(COS + (size_t)row * 16 + ib + 4);
;                         const f32x4 s0 = *(const f32x4*)(SIN + (size_t)row * 16 + ib), s1 = *(const f32x4*)(SIN + (size_t)row * 16 + ib + 4);
;                         f32x4 p0, p1;
; #pragma unroll
;                         for (int i = 0; i < 4; ++i) { p0[i] = xor32(v0[i]); p1[i] = xor32(v1[i]); }
;                         const float sg = (fq < 2) ? -1.f : 1.f;
;                         v0 = v0 * c0 + p0 * s0 * sg; v1 = v1 * c1 + p1 * s1 * sg;
;                     }
;                     *(u32x4*)(QM + (size_t)row * 768 + c) = pack8(v0, v1);
.LBB0_668:
	v_cvt_pk_bf16_f32 v82, v86, v87
	v_cvt_pk_bf16_f32 v83, v88, v89
	v_cvt_pk_bf16_f32 v84, v98, v99
	v_cvt_pk_bf16_f32 v85, v92, v93
	global_store_dwordx4 v[90:91], v[82:85], off offset:256
	ds_read_b32 v82, v151 offset:384
	s_and_b64 vcc, exec, s[12:13]
	v_add3_u32 v84, s3, v152, 48
	v_ashrrev_i32_e32 v85, 31, v84
	v_lshlrev_b64 v[94:95], 4, v[84:85]
	s_waitcnt lgkmcnt(0)
	v_pk_mul_f32 v[92:93], v[74:75], v[82:83] op_sel_hi:[1,0]
	v_lshlrev_b64 v[74:75], 2, v[94:95]
	v_pk_mul_f32 v[86:87], v[80:81], v[82:83] op_sel_hi:[1,0]
	v_pk_mul_f32 v[88:89], v[78:79], v[82:83] op_sel_hi:[1,0]
	v_pk_mul_f32 v[90:91], v[76:77], v[82:83] op_sel_hi:[1,0]
	v_lshl_add_u64 v[80:81], s[26:27], 0, v[74:75]
	v_lshl_add_u64 v[78:79], s[28:29], 0, v[74:75]
	s_cbranch_vccnz .LBB0_670
	v_lshl_add_u64 v[74:75], v[80:81], 0, v[0:1]
	v_lshl_add_u64 v[102:103], v[78:79], 0, v[0:1]
	s_waitcnt vmcnt(14)
	v_mov_b32_e32 v94, v194
	v_mov_b32_e32 v95, v195
	v_mov_b32_e32 v96, v196
	v_mov_b32_e32 v97, v197
	v_mov_b32_e32 v74, v198
	v_mov_b32_e32 v75, v199
	v_mov_b32_e32 v76, v200
	v_mov_b32_e32 v77, v201
	v_mov_b32_e32 v98, v202
	v_mov_b32_e32 v99, v203
	v_mov_b32_e32 v100, v204
	v_mov_b32_e32 v101, v205
	v_mov_b32_e32 v102, v206
	v_mov_b32_e32 v103, v207
	v_mov_b32_e32 v104, v208
	v_mov_b32_e32 v105, v209
	global_load_dwordx4 v[194:197], v[244:245], off offset:2048
	global_load_dwordx4 v[198:201], v[244:245], off offset:2064
	global_load_dwordx4 v[202:205], v[246:247], off offset:2048
	global_load_dwordx4 v[206:209], v[246:247], off offset:2064
	v_mov_b32_e32 v83, v88
	v_mov_b32_e32 v85, v88
	s_nop 1
	v_permlane32_swap_b32_e32 v83, v85
	v_cndmask_b32_e64 v106, v83, v85, s[4:5]
	v_mov_b32_e32 v83, v92
	v_mov_b32_e32 v85, v92
	s_nop 1
	v_permlane32_swap_b32_e32 v83, v85
	v_cndmask_b32_e64 v108, v83, v85, s[4:5]
	v_mov_b32_e32 v83, v89
	v_mov_b32_e32 v85, v89
	s_nop 1
	v_permlane32_swap_b32_e32 v83, v85
	v_cndmask_b32_e64 v107, v83, v85, s[4:5]
	v_mov_b32_e32 v83, v93
	v_mov_b32_e32 v85, v93
	s_nop 1
	v_permlane32_swap_b32_e32 v83, v85
	v_cndmask_b32_e64 v109, v83, v85, s[4:5]
	v_mov_b32_e32 v83, v86
	v_mov_b32_e32 v85, v86
	s_nop 1
	v_permlane32_swap_b32_e32 v83, v85
	v_cndmask_b32_e64 v110, v83, v85, s[4:5]
	v_mov_b32_e32 v83, v90
	v_mov_b32_e32 v85, v90
	s_nop 1
	v_permlane32_swap_b32_e32 v83, v85
	v_cndmask_b32_e64 v112, v83, v85, s[4:5]
	v_mov_b32_e32 v83, v87
	v_mov_b32_e32 v85, v87
	s_nop 1
	v_permlane32_swap_b32_e32 v83, v85
	v_cndmask_b32_e64 v111, v83, v85, s[4:5]
	v_mov_b32_e32 v83, v91
	v_mov_b32_e32 v85, v91
	s_nop 1
	v_permlane32_swap_b32_e32 v83, v85
	v_cndmask_b32_e64 v113, v83, v85, s[4:5]
	s_waitcnt lgkmcnt(0)
	v_pk_mul_f32 v[100:101], v[100:101], v[110:111]
	v_pk_mul_f32 v[98:99], v[98:99], v[106:107]
	v_mov_b32_e32 v106, v134
	v_mov_b32_e32 v107, v134
	v_pk_mul_f32 v[98:99], v[134:135], v[98:99]
	v_pk_mul_f32 v[100:101], v[106:107], v[100:101]
	v_pk_fma_f32 v[88:89], v[88:89], v[94:95], v[98:99]
	v_pk_fma_f32 v[86:87], v[86:87], v[96:97], v[100:101]
	v_pk_mul_f32 v[94:95], v[104:105], v[112:113]
	v_pk_mul_f32 v[96:97], v[102:103], v[108:109]
	v_pk_mul_f32 v[94:95], v[106:107], v[94:95]
	v_pk_mul_f32 v[96:97], v[134:135], v[96:97]
	v_pk_fma_f32 v[90:91], v[90:91], v[76:77], v[94:95]
	v_pk_fma_f32 v[92:93], v[92:93], v[74:75], v[96:97]
.LBB0_670:
	v_mov_b64_e32 v[74:75], s[22:23]
	s_movk_i32 s3, 0x600
	v_mov_b32_e32 v83, v82
	v_mad_i64_i32 v[74:75], s[6:7], v84, s3, v[74:75]
	v_mov_b32_e32 v76, v82
	v_mov_b32_e32 v77, v82
	v_cvt_pk_bf16_f32 v94, v88, v89
	v_cvt_pk_bf16_f32 v95, v86, v87
	v_cvt_pk_bf16_f32 v96, v92, v93
	v_cvt_pk_bf16_f32 v97, v90, v91
	v_lshl_add_u64 v[74:75], v[122:123], 1, v[74:75]
	v_pk_mul_f32 v[72:73], v[72:73], v[76:77]
	v_pk_mul_f32 v[70:71], v[70:71], v[82:83]
	v_pk_mul_f32 v[76:77], v[68:69], v[76:77]
	s_and_b64 vcc, exec, s[14:15]
	v_pk_mul_f32 v[82:83], v[66:67], v[82:83]
	global_store_dwordx4 v[74:75], v[94:97], off
	s_cbranch_vccnz .LBB0_672
	v_lshl_add_u64 v[66:67], v[80:81], 0, v[0:1]
	v_lshl_add_u64 v[88:89], v[78:79], 0, v[0:1]
	s_waitcnt vmcnt(14)
	v_mov_b32_e32 v84, v194
	v_mov_b32_e32 v85, v195
	v_mov_b32_e32 v86, v196
	v_mov_b32_e32 v87, v197
	v_mov_b32_e32 v66, v198
	v_mov_b32_e32 v67, v199
	v_mov_b32_e32 v68, v200
	v_mov_b32_e32 v69, v201
	v_mov_b32_e32 v78, v202
	v_mov_b32_e32 v79, v203
	v_mov_b32_e32 v80, v204
	v_mov_b32_e32 v81, v205
	v_mov_b32_e32 v88, v206
	v_mov_b32_e32 v89, v207
	v_mov_b32_e32 v90, v208
	v_mov_b32_e32 v91, v209
	global_load_dwordx4 v[194:197], v[244:245], off offset:2048
	global_load_dwordx4 v[198:201], v[244:245], off offset:2064
	global_load_dwordx4 v[202:205], v[246:247], off offset:2048
	global_load_dwordx4 v[206:209], v[246:247], off offset:2064
	v_mov_b32_e32 v92, v70
	v_mov_b32_e32 v93, v70
	s_nop 1
	v_permlane32_swap_b32_e32 v92, v93
	v_cndmask_b32_e64 v92, v92, v93, s[4:5]
	v_mov_b32_e32 v93, v82
	v_mov_b32_e32 v94, v82
	s_nop 1
	v_permlane32_swap_b32_e32 v93, v94
	v_cndmask_b32_e64 v94, v93, v94, s[4:5]
	v_mov_b32_e32 v93, v71
	v_mov_b32_e32 v95, v71
	s_nop 1
	v_permlane32_swap_b32_e32 v93, v95
	v_cndmask_b32_e64 v93, v93, v95, s[4:5]
	v_mov_b32_e32 v95, v83
	v_mov_b32_e32 v96, v83
	s_nop 1
	v_permlane32_swap_b32_e32 v95, v96
	v_cndmask_b32_e64 v95, v95, v96, s[4:5]
	v_mov_b32_e32 v96, v72
	v_mov_b32_e32 v97, v72
	s_nop 1
	v_permlane32_swap_b32_e32 v96, v97
	v_cndmask_b32_e64 v96, v96, v97, s[4:5]
	v_mov_b32_e32 v97, v76
	v_mov_b32_e32 v98, v76
	s_nop 1
	v_permlane32_swap_b32_e32 v97, v98
	v_cndmask_b32_e64 v98, v97, v98, s[4:5]
	v_mov_b32_e32 v97, v73
	v_mov_b32_e32 v99, v73
	s_nop 1
	v_permlane32_swap_b32_e32 v97, v99
	v_cndmask_b32_e64 v97, v97, v99, s[4:5]
	v_mov_b32_e32 v99, v77
	v_mov_b32_e32 v100, v77
	s_nop 1
	v_permlane32_swap_b32_e32 v99, v100
	v_cndmask_b32_e64 v99, v99, v100, s[4:5]
	s_waitcnt lgkmcnt(0)
	v_pk_mul_f32 v[80:81], v[80:81], v[96:97]
	v_pk_mul_f32 v[78:79], v[78:79], v[92:93]
	v_mov_b32_e32 v92, v134
	v_mov_b32_e32 v93, v134
	v_pk_mul_f32 v[78:79], v[134:135], v[78:79]
	v_pk_mul_f32 v[80:81], v[92:93], v[80:81]
	v_pk_fma_f32 v[70:71], v[70:71], v[84:85], v[78:79]
	v_pk_fma_f32 v[72:73], v[72:73], v[86:87], v[80:81]
	v_pk_mul_f32 v[78:79], v[90:91], v[98:99]
	v_pk_mul_f32 v[80:81], v[88:89], v[94:95]
	v_pk_mul_f32 v[78:79], v[92:93], v[78:79]
	v_pk_mul_f32 v[80:81], v[134:135], v[80:81]
	v_pk_fma_f32 v[76:77], v[76:77], v[68:69], v[78:79]
	v_pk_fma_f32 v[82:83], v[82:83], v[66:67], v[80:81]
; __device__ __forceinline__ float xor32(float x) { auto rr = __builtin_amdgcn_permlane32_swap(__float_as_uint(x), __float_as_uint(x), false, false); return __uint_as_float(((unsigned)(threadIdx.x & 32)) ? rr[0] : rr[1]); }
; __device__ __forceinline__ u32x4 pack8(f32x4 a, f32x4 b) { u32x4 w; w.x = pk2(a[0], a[1]); w.y = pk2(a[2], a[3]); w.z = pk2(b[0], b[1]); w.w = pk2(b[2], b[3]); return w; }
;     __device__ __forceinline__ void operator()(const f32x4 (&acc)[2][2][4][2], const Unit& u, int ui, int wr, int wc, int fr, int fq, LAS unsigned char* lds) const {
;     ...
;                     const int c = u.pn * 256 + bj * 128 + wc * 32 + fq * 8; const int g32 = u.pn * 8 + bj * 4 + wc;
;                     f32x4 v0 = acc[ai][bj][m][0] * rs, v1 = acc[ai][bj][m][1] * rs;
;                     if ((g32 % 3) == 2) {
;                         const int ib = 8 * (fq & 1);
;                         const f32x4 c0 = *(const f32x4*)(COS + (size_t)row * 16 + ib), c1 = *(const f32x4*)(COS + (size_t)row * 16 + ib + 4);
;                         const f32x4 s0 = *(const f32x4*)(SIN + (size_t)row * 16 + ib), s1 = *(const f32x4*)(SIN + (size_t)row * 16 + ib + 4);
;                         f32x4 p0, p1;
; #pragma unroll
;                         for (int i = 0; i < 4; ++i) { p0[i] = xor32(v0[i]); p1[i] = xor32(v1[i]); }
;                         const float sg = (fq < 2) ? -1.f : 1.f;
;                         v0 = v0 * c0 + p0 * s0 * sg; v1 = v1 * c1 + p1 * s1 * sg;
;                     }
;                     *(u32x4*)(QM + (size_t)row * 768 + c) = pack8(v0, v1);
.LBB0_672:
	v_cvt_pk_bf16_f32 v66, v70, v71
	v_cvt_pk_bf16_f32 v67, v72, v73
	v_cvt_pk_bf16_f32 v68, v82, v83
	v_cvt_pk_bf16_f32 v69, v76, v77
	global_store_dwordx4 v[74:75], v[66:69], off offset:256
	ds_read_b32 v66, v151 offset:1024
	s_and_b64 vcc, exec, s[12:13]
	v_add_u32_e32 v68, 0x80, v136
	v_ashrrev_i32_e32 v69, 31, v68
	v_lshlrev_b64 v[78:79], 4, v[68:69]
	s_waitcnt lgkmcnt(0)
	v_pk_mul_f32 v[76:77], v[58:59], v[66:67] op_sel_hi:[1,0]
	v_lshlrev_b64 v[58:59], 2, v[78:79]
	v_pk_mul_f32 v[70:71], v[64:65], v[66:67] op_sel_hi:[1,0]
	v_pk_mul_f32 v[72:73], v[62:63], v[66:67] op_sel_hi:[1,0]
	v_pk_mul_f32 v[74:75], v[60:61], v[66:67] op_sel_hi:[1,0]
	v_lshl_add_u64 v[64:65], s[26:27], 0, v[58:59]
	v_lshl_add_u64 v[62:63], s[28:29], 0, v[58:59]
	s_cbranch_vccnz .LBB0_674
	v_lshl_add_u64 v[58:59], v[64:65], 0, v[0:1]
	v_lshl_add_u64 v[86:87], v[62:63], 0, v[0:1]
	s_waitcnt vmcnt(14)
	v_mov_b32_e32 v78, v214
	v_mov_b32_e32 v79, v215
	v_mov_b32_e32 v80, v216
	v_mov_b32_e32 v81, v217
	v_mov_b32_e32 v58, v218
	v_mov_b32_e32 v59, v219
	v_mov_b32_e32 v60, v220
	v_mov_b32_e32 v61, v221
	v_mov_b32_e32 v82, v222
	v_mov_b32_e32 v83, v223
	v_mov_b32_e32 v84, v224
	v_mov_b32_e32 v85, v225
	v_mov_b32_e32 v86, v226
	v_mov_b32_e32 v87, v227
	v_mov_b32_e32 v88, v228
	v_mov_b32_e32 v89, v229
	global_load_dwordx4 v[214:217], v[244:245], off offset:3072
	global_load_dwordx4 v[218:221], v[244:245], off offset:3088
	global_load_dwordx4 v[222:225], v[246:247], off offset:3072
	global_load_dwordx4 v[226:229], v[246:247], off offset:3088
	v_mov_b32_e32 v67, v72
	v_mov_b32_e32 v69, v72
	s_nop 1
	v_permlane32_swap_b32_e32 v67, v69
	v_cndmask_b32_e64 v90, v67, v69, s[4:5]
	v_mov_b32_e32 v67, v76
	v_mov_b32_e32 v69, v76
	s_nop 1
	v_permlane32_swap_b32_e32 v67, v69
	v_cndmask_b32_e64 v92, v67, v69, s[4:5]
	v_mov_b32_e32 v67, v73
	v_mov_b32_e32 v69, v73
	s_nop 1
	v_permlane32_swap_b32_e32 v67, v69
	v_cndmask_b32_e64 v91, v67, v69, s[4:5]
	v_mov_b32_e32 v67, v77
	v_mov_b32_e32 v69, v77
	s_nop 1
	v_permlane32_swap_b32_e32 v67, v69
	v_cndmask_b32_e64 v93, v67, v69, s[4:5]
	v_mov_b32_e32 v67, v70
	v_mov_b32_e32 v69, v70
	s_nop 1
	v_permlane32_swap_b32_e32 v67, v69
	v_cndmask_b32_e64 v94, v67, v69, s[4:5]
	v_mov_b32_e32 v67, v74
	v_mov_b32_e32 v69, v74
	s_nop 1
	v_permlane32_swap_b32_e32 v67, v69
	v_cndmask_b32_e64 v96, v67, v69, s[4:5]
	v_mov_b32_e32 v67, v71
	v_mov_b32_e32 v69, v71
	s_nop 1
	v_permlane32_swap_b32_e32 v67, v69
	v_cndmask_b32_e64 v95, v67, v69, s[4:5]
	v_mov_b32_e32 v67, v75
	v_mov_b32_e32 v69, v75
	s_nop 1
	v_permlane32_swap_b32_e32 v67, v69
	v_cndmask_b32_e64 v97, v67, v69, s[4:5]
	s_waitcnt lgkmcnt(0)
	v_pk_mul_f32 v[84:85], v[84:85], v[94:95]
	v_pk_mul_f32 v[82:83], v[82:83], v[90:91]
	v_mov_b32_e32 v90, v134
	v_mov_b32_e32 v91, v134
	v_pk_mul_f32 v[82:83], v[134:135], v[82:83]
	v_pk_mul_f32 v[84:85], v[90:91], v[84:85]
	v_pk_fma_f32 v[72:73], v[72:73], v[78:79], v[82:83]
	v_pk_fma_f32 v[70:71], v[70:71], v[80:81], v[84:85]
	v_pk_mul_f32 v[78:79], v[88:89], v[96:97]
	v_pk_mul_f32 v[80:81], v[86:87], v[92:93]
	v_pk_mul_f32 v[78:79], v[90:91], v[78:79]
	v_pk_mul_f32 v[80:81], v[134:135], v[80:81]
	v_pk_fma_f32 v[74:75], v[74:75], v[60:61], v[78:79]
	v_pk_fma_f32 v[76:77], v[76:77], v[58:59], v[80:81]
.LBB0_674:
	v_mov_b64_e32 v[58:59], s[22:23]
	v_mov_b32_e32 v67, v66
	v_mad_i64_i32 v[58:59], s[6:7], v68, s3, v[58:59]
	v_mov_b32_e32 v60, v66
	v_mov_b32_e32 v61, v66
	v_cvt_pk_bf16_f32 v78, v72, v73
	v_cvt_pk_bf16_f32 v79, v70, v71
	v_cvt_pk_bf16_f32 v80, v76, v77
	v_cvt_pk_bf16_f32 v81, v74, v75
	v_lshl_add_u64 v[58:59], v[122:123], 1, v[58:59]
	v_pk_mul_f32 v[56:57], v[56:57], v[60:61]
	v_pk_mul_f32 v[54:55], v[54:55], v[66:67]
	v_pk_mul_f32 v[60:61], v[52:53], v[60:61]
	s_and_b64 vcc, exec, s[14:15]
	v_pk_mul_f32 v[66:67], v[50:51], v[66:67]
	global_store_dwordx4 v[58:59], v[78:81], off
	s_cbranch_vccnz .LBB0_676
	v_lshl_add_u64 v[50:51], v[64:65], 0, v[0:1]
	v_lshl_add_u64 v[72:73], v[62:63], 0, v[0:1]
	s_waitcnt vmcnt(14)
	v_mov_b32_e32 v68, v214
	v_mov_b32_e32 v69, v215
	v_mov_b32_e32 v70, v216
	v_mov_b32_e32 v71, v217
	v_mov_b32_e32 v50, v218
	v_mov_b32_e32 v51, v219
	v_mov_b32_e32 v52, v220
	v_mov_b32_e32 v53, v221
	v_mov_b32_e32 v62, v222
	v_mov_b32_e32 v63, v223
	v_mov_b32_e32 v64, v224
	v_mov_b32_e32 v65, v225
	v_mov_b32_e32 v72, v226
	v_mov_b32_e32 v73, v227
	v_mov_b32_e32 v74, v228
	v_mov_b32_e32 v75, v229
	global_load_dwordx4 v[214:217], v[244:245], off offset:3072
	global_load_dwordx4 v[218:221], v[244:245], off offset:3088
	global_load_dwordx4 v[222:225], v[246:247], off offset:3072
	global_load_dwordx4 v[226:229], v[246:247], off offset:3088
	v_mov_b32_e32 v76, v54
	v_mov_b32_e32 v77, v54
	s_nop 1
	v_permlane32_swap_b32_e32 v76, v77
	v_cndmask_b32_e64 v76, v76, v77, s[4:5]
	v_mov_b32_e32 v77, v66
	v_mov_b32_e32 v78, v66
	s_nop 1
	v_permlane32_swap_b32_e32 v77, v78
	v_cndmask_b32_e64 v78, v77, v78, s[4:5]
	v_mov_b32_e32 v77, v55
	v_mov_b32_e32 v79, v55
	s_nop 1
	v_permlane32_swap_b32_e32 v77, v79
	v_cndmask_b32_e64 v77, v77, v79, s[4:5]
	v_mov_b32_e32 v79, v67
	v_mov_b32_e32 v80, v67
	s_nop 1
	v_permlane32_swap_b32_e32 v79, v80
	v_cndmask_b32_e64 v79, v79, v80, s[4:5]
	v_mov_b32_e32 v80, v56
	v_mov_b32_e32 v81, v56
	s_nop 1
	v_permlane32_swap_b32_e32 v80, v81
	v_cndmask_b32_e64 v80, v80, v81, s[4:5]
	v_mov_b32_e32 v81, v60
	v_mov_b32_e32 v82, v60
	s_nop 1
	v_permlane32_swap_b32_e32 v81, v82
	v_cndmask_b32_e64 v82, v81, v82, s[4:5]
	v_mov_b32_e32 v81, v57
	v_mov_b32_e32 v83, v57
	s_nop 1
	v_permlane32_swap_b32_e32 v81, v83
	v_cndmask_b32_e64 v81, v81, v83, s[4:5]
	v_mov_b32_e32 v83, v61
	v_mov_b32_e32 v84, v61
	s_nop 1
	v_permlane32_swap_b32_e32 v83, v84
	v_cndmask_b32_e64 v83, v83, v84, s[4:5]
	s_waitcnt lgkmcnt(0)
	v_pk_mul_f32 v[64:65], v[64:65], v[80:81]
	v_pk_mul_f32 v[62:63], v[62:63], v[76:77]
	v_mov_b32_e32 v76, v134
	v_mov_b32_e32 v77, v134
	v_pk_mul_f32 v[62:63], v[134:135], v[62:63]
	v_pk_mul_f32 v[64:65], v[76:77], v[64:65]
	v_pk_fma_f32 v[54:55], v[54:55], v[68:69], v[62:63]
	v_pk_fma_f32 v[56:57], v[56:57], v[70:71], v[64:65]
	v_pk_mul_f32 v[62:63], v[74:75], v[82:83]
	v_pk_mul_f32 v[64:65], v[72:73], v[78:79]
	v_pk_mul_f32 v[62:63], v[76:77], v[62:63]
	v_pk_mul_f32 v[64:65], v[134:135], v[64:65]
	v_pk_fma_f32 v[60:61], v[60:61], v[52:53], v[62:63]
	v_pk_fma_f32 v[66:67], v[66:67], v[50:51], v[64:65]
; __device__ __forceinline__ float xor32(float x) { auto rr = __builtin_amdgcn_permlane32_swap(__float_as_uint(x), __float_as_uint(x), false, false); return __uint_as_float(((unsigned)(threadIdx.x & 32)) ? rr[0] : rr[1]); }
; __device__ __forceinline__ u32x4 pack8(f32x4 a, f32x4 b) { u32x4 w; w.x = pk2(a[0], a[1]); w.y = pk2(a[2], a[3]); w.z = pk2(b[0], b[1]); w.w = pk2(b[2], b[3]); return w; }
;     __device__ __forceinline__ void operator()(const f32x4 (&acc)[2][2][4][2], const Unit& u, int ui, int wr, int wc, int fr, int fq, LAS unsigned char* lds) const {
;     ...
;                     const int c = u.pn * 256 + bj * 128 + wc * 32 + fq * 8; const int g32 = u.pn * 8 + bj * 4 + wc;
;                     f32x4 v0 = acc[ai][bj][m][0] * rs, v1 = acc[ai][bj][m][1] * rs;
;                     if ((g32 % 3) == 2) {
;                         const int ib = 8 * (fq & 1);
;                         const f32x4 c0 = *(const f32x4*)(COS + (size_t)row * 16 + ib), c1 = *(const f32x4*)(COS + (size_t)row * 16 + ib + 4);
;                         const f32x4 s0 = *(const f32x4*)(SIN + (size_t)row * 16 + ib), s1 = *(const f32x4*)(SIN + (size_t)row * 16 + ib + 4);
;                         f32x4 p0, p1;
; #pragma unroll
;                         for (int i = 0; i < 4; ++i) { p0[i] = xor32(v0[i]); p1[i] = xor32(v1[i]); }
;                         const float sg = (fq < 2) ? -1.f : 1.f;
;                         v0 = v0 * c0 + p0 * s0 * sg; v1 = v1 * c1 + p1 * s1 * sg;
;                     }
;                     *(u32x4*)(QM + (size_t)row * 768 + c) = pack8(v0, v1);
.LBB0_676:
	v_cvt_pk_bf16_f32 v50, v54, v55
	v_cvt_pk_bf16_f32 v51, v56, v57
	v_cvt_pk_bf16_f32 v52, v66, v67
	v_cvt_pk_bf16_f32 v53, v60, v61
	global_store_dwordx4 v[58:59], v[50:53], off offset:256
	ds_read_b32 v50, v151 offset:1152
	s_and_b64 vcc, exec, s[12:13]
	v_add_u32_e32 v52, 0x90, v136
	v_ashrrev_i32_e32 v53, 31, v52
	v_lshlrev_b64 v[62:63], 4, v[52:53]
	s_waitcnt lgkmcnt(0)
	v_pk_mul_f32 v[60:61], v[42:43], v[50:51] op_sel_hi:[1,0]
	v_lshlrev_b64 v[42:43], 2, v[62:63]
	v_pk_mul_f32 v[54:55], v[48:49], v[50:51] op_sel_hi:[1,0]
	v_pk_mul_f32 v[56:57], v[46:47], v[50:51] op_sel_hi:[1,0]
	v_pk_mul_f32 v[58:59], v[44:45], v[50:51] op_sel_hi:[1,0]
	v_lshl_add_u64 v[48:49], s[26:27], 0, v[42:43]
	v_lshl_add_u64 v[46:47], s[28:29], 0, v[42:43]
	s_cbranch_vccnz .LBB0_678
	v_lshl_add_u64 v[42:43], v[48:49], 0, v[0:1]
	v_lshl_add_u64 v[70:71], v[46:47], 0, v[0:1]
	s_waitcnt vmcnt(14)
	v_mov_b32_e32 v62, v176
	v_mov_b32_e32 v63, v177
	v_mov_b32_e32 v64, v178
	v_mov_b32_e32 v65, v179
	v_mov_b32_e32 v42, v180
	v_mov_b32_e32 v43, v181
	v_mov_b32_e32 v44, v182
	v_mov_b32_e32 v45, v183
	v_mov_b32_e32 v66, v184
	v_mov_b32_e32 v67, v185
	v_mov_b32_e32 v68, v186
	v_mov_b32_e32 v69, v187
	v_mov_b32_e32 v70, v230
	v_mov_b32_e32 v71, v231
	v_mov_b32_e32 v72, v232
	v_mov_b32_e32 v73, v233
	v_mov_b32_e32 v51, v56
	v_mov_b32_e32 v53, v56
	s_nop 1
	v_permlane32_swap_b32_e32 v51, v53
	v_cndmask_b32_e64 v74, v51, v53, s[4:5]
	v_mov_b32_e32 v51, v60
	v_mov_b32_e32 v53, v60
	s_nop 1
	v_permlane32_swap_b32_e32 v51, v53
	v_cndmask_b32_e64 v76, v51, v53, s[4:5]
	v_mov_b32_e32 v51, v57
	v_mov_b32_e32 v53, v57
	s_nop 1
	v_permlane32_swap_b32_e32 v51, v53
	v_cndmask_b32_e64 v75, v51, v53, s[4:5]
	v_mov_b32_e32 v51, v61
	v_mov_b32_e32 v53, v61
	s_nop 1
	v_permlane32_swap_b32_e32 v51, v53
	v_cndmask_b32_e64 v77, v51, v53, s[4:5]
	v_mov_b32_e32 v51, v54
	v_mov_b32_e32 v53, v54
	s_nop 1
	v_permlane32_swap_b32_e32 v51, v53
	v_cndmask_b32_e64 v78, v51, v53, s[4:5]
	v_mov_b32_e32 v51, v58
	v_mov_b32_e32 v53, v58
	s_nop 1
	v_permlane32_swap_b32_e32 v51, v53
	v_cndmask_b32_e64 v80, v51, v53, s[4:5]
	v_mov_b32_e32 v51, v55
	v_mov_b32_e32 v53, v55
	s_nop 1
	v_permlane32_swap_b32_e32 v51, v53
	v_cndmask_b32_e64 v79, v51, v53, s[4:5]
	v_mov_b32_e32 v51, v59
	v_mov_b32_e32 v53, v59
	s_nop 1
	v_permlane32_swap_b32_e32 v51, v53
	v_cndmask_b32_e64 v81, v51, v53, s[4:5]
	s_waitcnt lgkmcnt(0)
	v_pk_mul_f32 v[68:69], v[68:69], v[78:79]
	v_pk_mul_f32 v[66:67], v[66:67], v[74:75]
	v_mov_b32_e32 v74, v134
	v_mov_b32_e32 v75, v134
	v_pk_mul_f32 v[66:67], v[134:135], v[66:67]
	v_pk_mul_f32 v[68:69], v[74:75], v[68:69]
	v_pk_fma_f32 v[56:57], v[56:57], v[62:63], v[66:67]
	v_pk_fma_f32 v[54:55], v[54:55], v[64:65], v[68:69]
	v_pk_mul_f32 v[62:63], v[72:73], v[80:81]
	v_pk_mul_f32 v[64:65], v[70:71], v[76:77]
	v_pk_mul_f32 v[62:63], v[74:75], v[62:63]
	v_pk_mul_f32 v[64:65], v[134:135], v[64:65]
	v_pk_fma_f32 v[58:59], v[58:59], v[44:45], v[62:63]
	v_pk_fma_f32 v[60:61], v[60:61], v[42:43], v[64:65]
.LBB0_678:
	v_mov_b64_e32 v[42:43], s[22:23]
	v_mov_b32_e32 v51, v50
	v_mad_i64_i32 v[42:43], s[6:7], v52, s3, v[42:43]
	v_mov_b32_e32 v44, v50
	v_mov_b32_e32 v45, v50
	v_cvt_pk_bf16_f32 v62, v56, v57
	v_cvt_pk_bf16_f32 v63, v54, v55
	v_cvt_pk_bf16_f32 v64, v60, v61
	v_cvt_pk_bf16_f32 v65, v58, v59
	v_lshl_add_u64 v[42:43], v[122:123], 1, v[42:43]
	v_pk_mul_f32 v[40:41], v[40:41], v[44:45]
	v_pk_mul_f32 v[38:39], v[38:39], v[50:51]
	v_pk_mul_f32 v[44:45], v[36:37], v[44:45]
	s_and_b64 vcc, exec, s[14:15]
	v_pk_mul_f32 v[50:51], v[34:35], v[50:51]
	global_store_dwordx4 v[42:43], v[62:65], off
	s_cbranch_vccnz .LBB0_680
	v_lshl_add_u64 v[34:35], v[48:49], 0, v[0:1]
	v_lshl_add_u64 v[56:57], v[46:47], 0, v[0:1]
	s_waitcnt vmcnt(14)
	v_mov_b32_e32 v52, v176
	v_mov_b32_e32 v53, v177
	v_mov_b32_e32 v54, v178
	v_mov_b32_e32 v55, v179
	v_mov_b32_e32 v34, v180
	v_mov_b32_e32 v35, v181
	v_mov_b32_e32 v36, v182
	v_mov_b32_e32 v37, v183
	v_mov_b32_e32 v46, v184
	v_mov_b32_e32 v47, v185
	v_mov_b32_e32 v48, v186
	v_mov_b32_e32 v49, v187
	v_mov_b32_e32 v56, v230
	v_mov_b32_e32 v57, v231
	v_mov_b32_e32 v58, v232
	v_mov_b32_e32 v59, v233
	v_mov_b32_e32 v60, v38
	v_mov_b32_e32 v61, v38
	s_nop 1
	v_permlane32_swap_b32_e32 v60, v61
	v_cndmask_b32_e64 v60, v60, v61, s[4:5]
	v_mov_b32_e32 v61, v50
	v_mov_b32_e32 v62, v50
	s_nop 1
	v_permlane32_swap_b32_e32 v61, v62
	v_cndmask_b32_e64 v62, v61, v62, s[4:5]
	v_mov_b32_e32 v61, v39
	v_mov_b32_e32 v63, v39
	s_nop 1
	v_permlane32_swap_b32_e32 v61, v63
	v_cndmask_b32_e64 v61, v61, v63, s[4:5]
	v_mov_b32_e32 v63, v51
	v_mov_b32_e32 v64, v51
	s_nop 1
	v_permlane32_swap_b32_e32 v63, v64
	v_cndmask_b32_e64 v63, v63, v64, s[4:5]
	v_mov_b32_e32 v64, v40
	v_mov_b32_e32 v65, v40
	s_nop 1
	v_permlane32_swap_b32_e32 v64, v65
	v_cndmask_b32_e64 v64, v64, v65, s[4:5]
	v_mov_b32_e32 v65, v44
	v_mov_b32_e32 v66, v44
	s_nop 1
	v_permlane32_swap_b32_e32 v65, v66
	v_cndmask_b32_e64 v66, v65, v66, s[4:5]
	v_mov_b32_e32 v65, v41
	v_mov_b32_e32 v67, v41
	s_nop 1
	v_permlane32_swap_b32_e32 v65, v67
	v_cndmask_b32_e64 v65, v65, v67, s[4:5]
	v_mov_b32_e32 v67, v45
	v_mov_b32_e32 v68, v45
	s_nop 1
	v_permlane32_swap_b32_e32 v67, v68
	v_cndmask_b32_e64 v67, v67, v68, s[4:5]
	s_waitcnt lgkmcnt(0)
	v_pk_mul_f32 v[48:49], v[48:49], v[64:65]
	v_pk_mul_f32 v[46:47], v[46:47], v[60:61]
	v_mov_b32_e32 v60, v134
	v_mov_b32_e32 v61, v134
	v_pk_mul_f32 v[46:47], v[134:135], v[46:47]
	v_pk_mul_f32 v[48:49], v[60:61], v[48:49]
	v_pk_fma_f32 v[38:39], v[38:39], v[52:53], v[46:47]
	v_pk_fma_f32 v[40:41], v[40:41], v[54:55], v[48:49]
	v_pk_mul_f32 v[46:47], v[58:59], v[66:67]
	v_pk_mul_f32 v[48:49], v[56:57], v[62:63]
	v_pk_mul_f32 v[46:47], v[60:61], v[46:47]
	v_pk_mul_f32 v[48:49], v[134:135], v[48:49]
	v_pk_fma_f32 v[44:45], v[44:45], v[36:37], v[46:47]
	v_pk_fma_f32 v[50:51], v[50:51], v[34:35], v[48:49]
; __device__ __forceinline__ float xor32(float x) { auto rr = __builtin_amdgcn_permlane32_swap(__float_as_uint(x), __float_as_uint(x), false, false); return __uint_as_float(((unsigned)(threadIdx.x & 32)) ? rr[0] : rr[1]); }
; __device__ __forceinline__ u32x4 pack8(f32x4 a, f32x4 b) { u32x4 w; w.x = pk2(a[0], a[1]); w.y = pk2(a[2], a[3]); w.z = pk2(b[0], b[1]); w.w = pk2(b[2], b[3]); return w; }
;     __device__ __forceinline__ void operator()(const f32x4 (&acc)[2][2][4][2], const Unit& u, int ui, int wr, int wc, int fr, int fq, LAS unsigned char* lds) const {
;     ...
;                     const int c = u.pn * 256 + bj * 128 + wc * 32 + fq * 8; const int g32 = u.pn * 8 + bj * 4 + wc;
;                     f32x4 v0 = acc[ai][bj][m][0] * rs, v1 = acc[ai][bj][m][1] * rs;
;                     if ((g32 % 3) == 2) {
;                         const int ib = 8 * (fq & 1);
;                         const f32x4 c0 = *(const f32x4*)(COS + (size_t)row * 16 + ib), c1 = *(const f32x4*)(COS + (size_t)row * 16 + ib + 4);
;                         const f32x4 s0 = *(const f32x4*)(SIN + (size_t)row * 16 + ib), s1 = *(const f32x4*)(SIN + (size_t)row * 16 + ib + 4);
;                         f32x4 p0, p1;
; #pragma unroll
;                         for (int i = 0; i < 4; ++i) { p0[i] = xor32(v0[i]); p1[i] = xor32(v1[i]); }
;                         const float sg = (fq < 2) ? -1.f : 1.f;
;                         v0 = v0 * c0 + p0 * s0 * sg; v1 = v1 * c1 + p1 * s1 * sg;
;                     }
;                     *(u32x4*)(QM + (size_t)row * 768 + c) = pack8(v0, v1);
.LBB0_680:
	v_cvt_pk_bf16_f32 v34, v38, v39
	v_cvt_pk_bf16_f32 v35, v40, v41
	v_cvt_pk_bf16_f32 v36, v50, v51
	v_cvt_pk_bf16_f32 v37, v44, v45
	global_store_dwordx4 v[42:43], v[34:37], off offset:256
	ds_read_b32 v34, v151 offset:1280
	s_and_b64 vcc, exec, s[12:13]
	v_add_u32_e32 v36, 0xa0, v136
	v_ashrrev_i32_e32 v37, 31, v36
	v_lshlrev_b64 v[46:47], 4, v[36:37]
	s_waitcnt lgkmcnt(0)
	v_pk_mul_f32 v[44:45], v[26:27], v[34:35] op_sel_hi:[1,0]
	v_lshlrev_b64 v[26:27], 2, v[46:47]
	v_pk_mul_f32 v[38:39], v[32:33], v[34:35] op_sel_hi:[1,0]
	v_pk_mul_f32 v[40:41], v[30:31], v[34:35] op_sel_hi:[1,0]
	v_pk_mul_f32 v[42:43], v[28:29], v[34:35] op_sel_hi:[1,0]
	v_lshl_add_u64 v[32:33], s[26:27], 0, v[26:27]
	v_lshl_add_u64 v[30:31], s[28:29], 0, v[26:27]
	s_cbranch_vccnz .LBB0_682
	v_lshl_add_u64 v[26:27], v[32:33], 0, v[0:1]
	v_lshl_add_u64 v[54:55], v[30:31], 0, v[0:1]
	s_waitcnt vmcnt(10)
	v_mov_b32_e32 v46, v194
	v_mov_b32_e32 v47, v195
	v_mov_b32_e32 v48, v196
	v_mov_b32_e32 v49, v197
	v_mov_b32_e32 v26, v198
	v_mov_b32_e32 v27, v199
	v_mov_b32_e32 v28, v200
	v_mov_b32_e32 v29, v201
	v_mov_b32_e32 v50, v202
	v_mov_b32_e32 v51, v203
	v_mov_b32_e32 v52, v204
	v_mov_b32_e32 v53, v205
	v_mov_b32_e32 v54, v206
	v_mov_b32_e32 v55, v207
	v_mov_b32_e32 v56, v208
	v_mov_b32_e32 v57, v209
	v_mov_b32_e32 v35, v40
	v_mov_b32_e32 v37, v40
	s_nop 1
	v_permlane32_swap_b32_e32 v35, v37
	v_cndmask_b32_e64 v58, v35, v37, s[4:5]
	v_mov_b32_e32 v35, v44
	v_mov_b32_e32 v37, v44
	s_nop 1
	v_permlane32_swap_b32_e32 v35, v37
	v_cndmask_b32_e64 v60, v35, v37, s[4:5]
	v_mov_b32_e32 v35, v41
	v_mov_b32_e32 v37, v41
	s_nop 1
	v_permlane32_swap_b32_e32 v35, v37
	v_cndmask_b32_e64 v59, v35, v37, s[4:5]
	v_mov_b32_e32 v35, v45
	v_mov_b32_e32 v37, v45
	s_nop 1
	v_permlane32_swap_b32_e32 v35, v37
	v_cndmask_b32_e64 v61, v35, v37, s[4:5]
	v_mov_b32_e32 v35, v38
	v_mov_b32_e32 v37, v38
	s_nop 1
	v_permlane32_swap_b32_e32 v35, v37
	v_cndmask_b32_e64 v62, v35, v37, s[4:5]
	v_mov_b32_e32 v35, v42
	v_mov_b32_e32 v37, v42
	s_nop 1
	v_permlane32_swap_b32_e32 v35, v37
	v_cndmask_b32_e64 v64, v35, v37, s[4:5]
	v_mov_b32_e32 v35, v39
	v_mov_b32_e32 v37, v39
	s_nop 1
	v_permlane32_swap_b32_e32 v35, v37
	v_cndmask_b32_e64 v63, v35, v37, s[4:5]
	v_mov_b32_e32 v35, v43
	v_mov_b32_e32 v37, v43
	s_nop 1
	v_permlane32_swap_b32_e32 v35, v37
	v_cndmask_b32_e64 v65, v35, v37, s[4:5]
	s_waitcnt lgkmcnt(0)
	v_pk_mul_f32 v[52:53], v[52:53], v[62:63]
	v_pk_mul_f32 v[50:51], v[50:51], v[58:59]
	v_mov_b32_e32 v58, v134
	v_mov_b32_e32 v59, v134
	v_pk_mul_f32 v[50:51], v[134:135], v[50:51]
	v_pk_mul_f32 v[52:53], v[58:59], v[52:53]
	v_pk_fma_f32 v[40:41], v[40:41], v[46:47], v[50:51]
	v_pk_fma_f32 v[38:39], v[38:39], v[48:49], v[52:53]
	v_pk_mul_f32 v[46:47], v[56:57], v[64:65]
	v_pk_mul_f32 v[48:49], v[54:55], v[60:61]
	v_pk_mul_f32 v[46:47], v[58:59], v[46:47]
	v_pk_mul_f32 v[48:49], v[134:135], v[48:49]
	v_pk_fma_f32 v[42:43], v[42:43], v[28:29], v[46:47]
	v_pk_fma_f32 v[44:45], v[44:45], v[26:27], v[48:49]
.LBB0_682:
	v_mov_b64_e32 v[26:27], s[22:23]
	v_mov_b32_e32 v35, v34
	v_mad_i64_i32 v[26:27], s[6:7], v36, s3, v[26:27]
	v_mov_b32_e32 v28, v34
	v_mov_b32_e32 v29, v34
	v_cvt_pk_bf16_f32 v46, v40, v41
	v_cvt_pk_bf16_f32 v47, v38, v39
	v_cvt_pk_bf16_f32 v48, v44, v45
	v_cvt_pk_bf16_f32 v49, v42, v43
	v_lshl_add_u64 v[26:27], v[122:123], 1, v[26:27]
	v_pk_mul_f32 v[24:25], v[24:25], v[28:29]
	v_pk_mul_f32 v[22:23], v[22:23], v[34:35]
	v_pk_mul_f32 v[28:29], v[20:21], v[28:29]
	s_and_b64 vcc, exec, s[14:15]
	v_pk_mul_f32 v[34:35], v[18:19], v[34:35]
	global_store_dwordx4 v[26:27], v[46:49], off
	s_cbranch_vccnz .LBB0_684
	v_lshl_add_u64 v[18:19], v[32:33], 0, v[0:1]
	v_lshl_add_u64 v[40:41], v[30:31], 0, v[0:1]
	s_waitcnt vmcnt(10)
	v_mov_b32_e32 v36, v194
	v_mov_b32_e32 v37, v195
	v_mov_b32_e32 v38, v196
	v_mov_b32_e32 v39, v197
	v_mov_b32_e32 v18, v198
	v_mov_b32_e32 v19, v199
	v_mov_b32_e32 v20, v200
	v_mov_b32_e32 v21, v201
	v_mov_b32_e32 v30, v202
	v_mov_b32_e32 v31, v203
	v_mov_b32_e32 v32, v204
	v_mov_b32_e32 v33, v205
	v_mov_b32_e32 v40, v206
	v_mov_b32_e32 v41, v207
	v_mov_b32_e32 v42, v208
	v_mov_b32_e32 v43, v209
	v_mov_b32_e32 v44, v22
	v_mov_b32_e32 v45, v22
	s_nop 1
	v_permlane32_swap_b32_e32 v44, v45
	v_cndmask_b32_e64 v44, v44, v45, s[4:5]
	v_mov_b32_e32 v45, v34
	v_mov_b32_e32 v46, v34
	s_nop 1
	v_permlane32_swap_b32_e32 v45, v46
	v_cndmask_b32_e64 v46, v45, v46, s[4:5]
	v_mov_b32_e32 v45, v23
	v_mov_b32_e32 v47, v23
	s_nop 1
	v_permlane32_swap_b32_e32 v45, v47
	v_cndmask_b32_e64 v45, v45, v47, s[4:5]
	v_mov_b32_e32 v47, v35
	v_mov_b32_e32 v48, v35
	s_nop 1
	v_permlane32_swap_b32_e32 v47, v48
	v_cndmask_b32_e64 v47, v47, v48, s[4:5]
	v_mov_b32_e32 v48, v24
	v_mov_b32_e32 v49, v24
	s_nop 1
	v_permlane32_swap_b32_e32 v48, v49
	v_cndmask_b32_e64 v48, v48, v49, s[4:5]
	v_mov_b32_e32 v49, v28
	v_mov_b32_e32 v50, v28
	s_nop 1
	v_permlane32_swap_b32_e32 v49, v50
	v_cndmask_b32_e64 v50, v49, v50, s[4:5]
	v_mov_b32_e32 v49, v25
	v_mov_b32_e32 v51, v25
	s_nop 1
	v_permlane32_swap_b32_e32 v49, v51
	v_cndmask_b32_e64 v49, v49, v51, s[4:5]
	v_mov_b32_e32 v51, v29
	v_mov_b32_e32 v52, v29
	s_nop 1
	v_permlane32_swap_b32_e32 v51, v52
	v_cndmask_b32_e64 v51, v51, v52, s[4:5]
	s_waitcnt lgkmcnt(0)
	v_pk_mul_f32 v[32:33], v[32:33], v[48:49]
	v_pk_mul_f32 v[30:31], v[30:31], v[44:45]
	v_mov_b32_e32 v44, v134
	v_mov_b32_e32 v45, v134
	v_pk_mul_f32 v[30:31], v[134:135], v[30:31]
	v_pk_mul_f32 v[32:33], v[44:45], v[32:33]
	v_pk_fma_f32 v[22:23], v[22:23], v[36:37], v[30:31]
	v_pk_fma_f32 v[24:25], v[24:25], v[38:39], v[32:33]
	v_pk_mul_f32 v[30:31], v[42:43], v[50:51]
	v_pk_mul_f32 v[32:33], v[40:41], v[46:47]
	v_pk_mul_f32 v[30:31], v[44:45], v[30:31]
	v_pk_mul_f32 v[32:33], v[134:135], v[32:33]
	v_pk_fma_f32 v[28:29], v[28:29], v[20:21], v[30:31]
	v_pk_fma_f32 v[34:35], v[34:35], v[18:19], v[32:33]
; __device__ __forceinline__ float xor32(float x) { auto rr = __builtin_amdgcn_permlane32_swap(__float_as_uint(x), __float_as_uint(x), false, false); return __uint_as_float(((unsigned)(threadIdx.x & 32)) ? rr[0] : rr[1]); }
; __device__ __forceinline__ u32x4 pack8(f32x4 a, f32x4 b) { u32x4 w; w.x = pk2(a[0], a[1]); w.y = pk2(a[2], a[3]); w.z = pk2(b[0], b[1]); w.w = pk2(b[2], b[3]); return w; }
;     __device__ __forceinline__ void operator()(const f32x4 (&acc)[2][2][4][2], const Unit& u, int ui, int wr, int wc, int fr, int fq, LAS unsigned char* lds) const {
;     ...
;                     const int c = u.pn * 256 + bj * 128 + wc * 32 + fq * 8; const int g32 = u.pn * 8 + bj * 4 + wc;
;                     f32x4 v0 = acc[ai][bj][m][0] * rs, v1 = acc[ai][bj][m][1] * rs;
;                     if ((g32 % 3) == 2) {
;                         const int ib = 8 * (fq & 1);
;                         const f32x4 c0 = *(const f32x4*)(COS + (size_t)row * 16 + ib), c1 = *(const f32x4*)(COS + (size_t)row * 16 + ib + 4);
;                         const f32x4 s0 = *(const f32x4*)(SIN + (size_t)row * 16 + ib), s1 = *(const f32x4*)(SIN + (size_t)row * 16 + ib + 4);
;                         f32x4 p0, p1;
; #pragma unroll
;                         for (int i = 0; i < 4; ++i) { p0[i] = xor32(v0[i]); p1[i] = xor32(v1[i]); }
;                         const float sg = (fq < 2) ? -1.f : 1.f;
;                         v0 = v0 * c0 + p0 * s0 * sg; v1 = v1 * c1 + p1 * s1 * sg;
;                     }
;                     *(u32x4*)(QM + (size_t)row * 768 + c) = pack8(v0, v1);
.LBB0_684:
	v_cvt_pk_bf16_f32 v18, v22, v23
	v_cvt_pk_bf16_f32 v19, v24, v25
	v_cvt_pk_bf16_f32 v20, v34, v35
	v_cvt_pk_bf16_f32 v21, v28, v29
	global_store_dwordx4 v[26:27], v[18:21], off offset:256
	ds_read_b32 v18, v151 offset:1408
	s_and_b64 vcc, exec, s[12:13]
	v_add_u32_e32 v20, 0xb0, v136
	v_ashrrev_i32_e32 v21, 31, v20
	v_lshlrev_b64 v[30:31], 4, v[20:21]
	s_waitcnt lgkmcnt(0)
	v_pk_mul_f32 v[28:29], v[10:11], v[18:19] op_sel_hi:[1,0]
	v_lshlrev_b64 v[10:11], 2, v[30:31]
	v_pk_mul_f32 v[22:23], v[16:17], v[18:19] op_sel_hi:[1,0]
	v_pk_mul_f32 v[24:25], v[14:15], v[18:19] op_sel_hi:[1,0]
	v_pk_mul_f32 v[26:27], v[12:13], v[18:19] op_sel_hi:[1,0]
	v_lshl_add_u64 v[16:17], s[26:27], 0, v[10:11]
	v_lshl_add_u64 v[14:15], s[28:29], 0, v[10:11]
	s_cbranch_vccnz .LBB0_686
	v_lshl_add_u64 v[10:11], v[16:17], 0, v[0:1]
	v_lshl_add_u64 v[38:39], v[14:15], 0, v[0:1]
	s_waitcnt vmcnt(6)
	v_mov_b32_e32 v30, v214
	v_mov_b32_e32 v31, v215
	v_mov_b32_e32 v32, v216
	v_mov_b32_e32 v33, v217
	v_mov_b32_e32 v10, v218
	v_mov_b32_e32 v11, v219
	v_mov_b32_e32 v12, v220
	v_mov_b32_e32 v13, v221
	v_mov_b32_e32 v34, v222
	v_mov_b32_e32 v35, v223
	v_mov_b32_e32 v36, v224
	v_mov_b32_e32 v37, v225
	v_mov_b32_e32 v38, v226
	v_mov_b32_e32 v39, v227
	v_mov_b32_e32 v40, v228
	v_mov_b32_e32 v41, v229
	v_mov_b32_e32 v19, v24
	v_mov_b32_e32 v21, v24
	s_nop 1
	v_permlane32_swap_b32_e32 v19, v21
	v_cndmask_b32_e64 v42, v19, v21, s[4:5]
	v_mov_b32_e32 v19, v28
	v_mov_b32_e32 v21, v28
	s_nop 1
	v_permlane32_swap_b32_e32 v19, v21
	v_cndmask_b32_e64 v44, v19, v21, s[4:5]
	v_mov_b32_e32 v19, v25
	v_mov_b32_e32 v21, v25
	s_nop 1
	v_permlane32_swap_b32_e32 v19, v21
	v_cndmask_b32_e64 v43, v19, v21, s[4:5]
	v_mov_b32_e32 v19, v29
	v_mov_b32_e32 v21, v29
	s_nop 1
	v_permlane32_swap_b32_e32 v19, v21
	v_cndmask_b32_e64 v45, v19, v21, s[4:5]
	v_mov_b32_e32 v19, v22
	v_mov_b32_e32 v21, v22
	s_nop 1
	v_permlane32_swap_b32_e32 v19, v21
	v_cndmask_b32_e64 v46, v19, v21, s[4:5]
	v_mov_b32_e32 v19, v26
	v_mov_b32_e32 v21, v26
	s_nop 1
	v_permlane32_swap_b32_e32 v19, v21
	v_cndmask_b32_e64 v48, v19, v21, s[4:5]
	v_mov_b32_e32 v19, v23
	v_mov_b32_e32 v21, v23
	s_nop 1
	v_permlane32_swap_b32_e32 v19, v21
	v_cndmask_b32_e64 v47, v19, v21, s[4:5]
	v_mov_b32_e32 v19, v27
	v_mov_b32_e32 v21, v27
	s_nop 1
	v_permlane32_swap_b32_e32 v19, v21
	v_cndmask_b32_e64 v49, v19, v21, s[4:5]
	s_waitcnt lgkmcnt(0)
	v_pk_mul_f32 v[36:37], v[36:37], v[46:47]
	v_pk_mul_f32 v[34:35], v[34:35], v[42:43]
	v_mov_b32_e32 v42, v134
	v_mov_b32_e32 v43, v134
	v_pk_mul_f32 v[34:35], v[134:135], v[34:35]
	v_pk_mul_f32 v[36:37], v[42:43], v[36:37]
	v_pk_fma_f32 v[24:25], v[24:25], v[30:31], v[34:35]
	v_pk_fma_f32 v[22:23], v[22:23], v[32:33], v[36:37]
	v_pk_mul_f32 v[30:31], v[40:41], v[48:49]
	v_pk_mul_f32 v[32:33], v[38:39], v[44:45]
	v_pk_mul_f32 v[30:31], v[42:43], v[30:31]
	v_pk_mul_f32 v[32:33], v[134:135], v[32:33]
	v_pk_fma_f32 v[26:27], v[26:27], v[12:13], v[30:31]
	v_pk_fma_f32 v[28:29], v[28:29], v[10:11], v[32:33]
.LBB0_686:
	v_mov_b64_e32 v[10:11], s[22:23]
	v_mov_b32_e32 v19, v18
	v_mad_i64_i32 v[10:11], s[6:7], v20, s3, v[10:11]
	v_mov_b32_e32 v12, v18
	v_mov_b32_e32 v13, v18
	v_cvt_pk_bf16_f32 v30, v24, v25
	v_cvt_pk_bf16_f32 v31, v22, v23
	v_cvt_pk_bf16_f32 v32, v28, v29
	v_cvt_pk_bf16_f32 v33, v26, v27
	v_lshl_add_u64 v[10:11], v[122:123], 1, v[10:11]
	v_pk_mul_f32 v[8:9], v[8:9], v[12:13]
	v_pk_mul_f32 v[6:7], v[6:7], v[18:19]
	v_pk_mul_f32 v[12:13], v[4:5], v[12:13]
	s_and_b64 vcc, exec, s[14:15]
	v_pk_mul_f32 v[18:19], v[2:3], v[18:19]
	global_store_dwordx4 v[10:11], v[30:33], off
	s_cbranch_vccnz .LBB0_688
	v_lshl_add_u64 v[2:3], v[16:17], 0, v[0:1]
	v_lshl_add_u64 v[24:25], v[14:15], 0, v[0:1]
	s_waitcnt vmcnt(6)
	v_mov_b32_e32 v20, v214
	v_mov_b32_e32 v21, v215
	v_mov_b32_e32 v22, v216
	v_mov_b32_e32 v23, v217
	v_mov_b32_e32 v2, v218
	v_mov_b32_e32 v3, v219
	v_mov_b32_e32 v4, v220
	v_mov_b32_e32 v5, v221
	v_mov_b32_e32 v14, v222
	v_mov_b32_e32 v15, v223
	v_mov_b32_e32 v16, v224
	v_mov_b32_e32 v17, v225
	v_mov_b32_e32 v24, v226
	v_mov_b32_e32 v25, v227
	v_mov_b32_e32 v26, v228
	v_mov_b32_e32 v27, v229
	v_mov_b32_e32 v0, v6
	v_mov_b32_e32 v28, v6
	s_nop 1
	v_permlane32_swap_b32_e32 v0, v28
	v_cndmask_b32_e64 v28, v0, v28, s[4:5]
	v_mov_b32_e32 v0, v18
	v_mov_b32_e32 v29, v18
	s_nop 1
	v_permlane32_swap_b32_e32 v0, v29
	v_cndmask_b32_e64 v30, v0, v29, s[4:5]
	v_mov_b32_e32 v0, v7
	v_mov_b32_e32 v29, v7
	s_nop 1
	v_permlane32_swap_b32_e32 v0, v29
	v_cndmask_b32_e64 v29, v0, v29, s[4:5]
	v_mov_b32_e32 v0, v19
	v_mov_b32_e32 v31, v19
	s_nop 1
	v_permlane32_swap_b32_e32 v0, v31
	v_cndmask_b32_e64 v31, v0, v31, s[4:5]
	v_mov_b32_e32 v0, v8
	v_mov_b32_e32 v32, v8
	s_nop 1
	v_permlane32_swap_b32_e32 v0, v32
	v_cndmask_b32_e64 v32, v0, v32, s[4:5]
	v_mov_b32_e32 v0, v12
	v_mov_b32_e32 v33, v12
	s_nop 1
	v_permlane32_swap_b32_e32 v0, v33
	v_cndmask_b32_e64 v34, v0, v33, s[4:5]
	v_mov_b32_e32 v0, v9
	v_mov_b32_e32 v33, v9
	s_nop 1
	v_permlane32_swap_b32_e32 v0, v33
	v_cndmask_b32_e64 v33, v0, v33, s[4:5]
	v_mov_b32_e32 v0, v13
	v_mov_b32_e32 v35, v13
	s_nop 1
	v_permlane32_swap_b32_e32 v0, v35
	v_cndmask_b32_e64 v35, v0, v35, s[4:5]
	s_waitcnt lgkmcnt(0)
	v_pk_mul_f32 v[16:17], v[16:17], v[32:33]
	v_pk_mul_f32 v[14:15], v[14:15], v[28:29]
	v_mov_b32_e32 v28, v134
	v_mov_b32_e32 v29, v134
	v_pk_mul_f32 v[14:15], v[134:135], v[14:15]
	v_pk_mul_f32 v[16:17], v[28:29], v[16:17]
	v_pk_fma_f32 v[6:7], v[6:7], v[20:21], v[14:15]
	v_pk_fma_f32 v[8:9], v[8:9], v[22:23], v[16:17]
	v_pk_mul_f32 v[14:15], v[26:27], v[34:35]
	v_pk_mul_f32 v[16:17], v[24:25], v[30:31]
	v_pk_mul_f32 v[14:15], v[28:29], v[14:15]
	v_pk_mul_f32 v[16:17], v[134:135], v[16:17]
	v_pk_fma_f32 v[12:13], v[12:13], v[4:5], v[14:15]
	v_pk_fma_f32 v[18:19], v[18:19], v[2:3], v[16:17]
